# baseline (speedup 1.0000x reference)
.Lc_go:
	s_cmp_eq_u32 s45, 0
	s_cbranch_scc0 .Lc_par1
	ds_read2_b64 v[48:51], v32 offset0:0 offset1:202
	ds_read2_b64 v[52:55], v32 offset0:1 offset1:203
	ds_read_b128 v[120:123], v33 offset:0
	ds_read2_b64 v[10:13], v34 offset0:0 offset1:202
	ds_read2_b64 v[56:59], v32 offset0:2 offset1:204
	ds_read2_b64 v[60:63], v32 offset0:3 offset1:205
	ds_read_b128 v[124:127], v33 offset:16
	ds_read2_b64 v[64:67], v32 offset0:4 offset1:206
	ds_read2_b64 v[68:71], v32 offset0:5 offset1:207
	ds_read_b128 v[128:131], v33 offset:32
	ds_read2_b64 v[72:75], v32 offset0:6 offset1:208
	s_mov_b32 s70, 0
	s_mov_b32 s71, 0
	s_waitcnt lgkmcnt(4)
.Lc0_loop:
	v_pk_fma_f16 v6, v2, v120, v121 op_sel:[0,0,0] op_sel_hi:[1,0,0] neg_lo:[1,0,0] neg_hi:[1,0,0]
	v_pk_fma_f16 v7, v3, v120, v121 op_sel:[0,0,0] op_sel_hi:[1,0,0] neg_lo:[1,0,0] neg_hi:[1,0,0]
	v_pk_fma_f16 v8, v4, v120, v121 op_sel:[0,0,0] op_sel_hi:[1,0,0] neg_lo:[1,0,0] neg_hi:[1,0,0]
	v_pk_fma_f16 v9, v5, v120, v121 op_sel:[0,0,0] op_sel_hi:[1,0,0] neg_lo:[1,0,0] neg_hi:[1,0,0]
	v_mfma_f32_16x16x32_f16 v[18:21], v[10:13], v[2:5], 0
	ds_read2_b64 v[76:79], v32 offset0:7 offset1:209
	ds_read_b128 v[132:135], v33 offset:48
	ds_read_b32 v37, v36 offset:4
	ds_read_b32 v38, v36 offset:68
	v_pk_fma_f16 v2, v48, v6, v2
	v_pk_fma_f16 v3, v49, v7, v3
	v_pk_fma_f16 v4, v50, v8, v4
	v_pk_fma_f16 v5, v51, v9, v5
	v_cndmask_b32_e64 v29, v29, v25, s[66:67]
	v_cvt_pk_f16_f32 v30, v26, v27
	v_cvt_pk_f16_f32 v31, v28, v29
	ds_write_b16 v39, v30 offset:0
	ds_write_b16_d16_hi v39, v30 offset:64
	ds_write_b16 v39, v31 offset:128
	ds_write_b16_d16_hi v39, v31 offset:192
	s_mov_b64 exec, 1
	ds_add_u32 v36, v44 offset:124
	s_mov_b64 exec, -1
	v_pk_fma_f16 v6, v2, v122, v123 op_sel:[0,0,0] op_sel_hi:[1,0,0] neg_lo:[1,0,0] neg_hi:[1,0,0]
	v_pk_fma_f16 v7, v3, v122, v123 op_sel:[0,0,0] op_sel_hi:[1,0,0] neg_lo:[1,0,0] neg_hi:[1,0,0]
	v_pk_fma_f16 v8, v4, v122, v123 op_sel:[0,0,0] op_sel_hi:[1,0,0] neg_lo:[1,0,0] neg_hi:[1,0,0]
	v_pk_fma_f16 v9, v5, v122, v123 op_sel:[0,0,0] op_sel_hi:[1,0,0] neg_lo:[1,0,0] neg_hi:[1,0,0]
	v_mfma_f32_16x16x32_f16 v[22:25], v[10:13], v[2:5], 0
	ds_read2_b64 v[80:83], v32 offset0:8 offset1:210
	v_pk_fma_f16 v2, v52, v6, v2
	v_pk_fma_f16 v3, v53, v7, v3
	v_pk_fma_f16 v4, v54, v8, v4
	v_pk_fma_f16 v5, v55, v9, v5
	v_cndmask_b32_e64 v26, v26, v18, s[60:61]
	v_pk_fma_f16 v6, v2, v124, v125 op_sel:[0,0,0] op_sel_hi:[1,0,0] neg_lo:[1,0,0] neg_hi:[1,0,0]
	v_pk_fma_f16 v7, v3, v124, v125 op_sel:[0,0,0] op_sel_hi:[1,0,0] neg_lo:[1,0,0] neg_hi:[1,0,0]
	v_pk_fma_f16 v8, v4, v124, v125 op_sel:[0,0,0] op_sel_hi:[1,0,0] neg_lo:[1,0,0] neg_hi:[1,0,0]
	v_pk_fma_f16 v9, v5, v124, v125 op_sel:[0,0,0] op_sel_hi:[1,0,0] neg_lo:[1,0,0] neg_hi:[1,0,0]
	v_mfma_f32_16x16x32_f16 v[18:21], v[10:13], v[2:5], 0
	ds_read2_b64 v[84:87], v32 offset0:9 offset1:211
	ds_read_b128 v[136:139], v33 offset:64
	v_pk_fma_f16 v2, v56, v6, v2
	v_pk_fma_f16 v3, v57, v7, v3
	v_pk_fma_f16 v4, v58, v8, v4
	v_pk_fma_f16 v5, v59, v9, v5
	v_cndmask_b32_e64 v27, v27, v23, s[60:61]
	v_pk_fma_f16 v6, v2, v126, v127 op_sel:[0,0,0] op_sel_hi:[1,0,0] neg_lo:[1,0,0] neg_hi:[1,0,0]
	v_pk_fma_f16 v7, v3, v126, v127 op_sel:[0,0,0] op_sel_hi:[1,0,0] neg_lo:[1,0,0] neg_hi:[1,0,0]
	v_pk_fma_f16 v8, v4, v126, v127 op_sel:[0,0,0] op_sel_hi:[1,0,0] neg_lo:[1,0,0] neg_hi:[1,0,0]
	v_pk_fma_f16 v9, v5, v126, v127 op_sel:[0,0,0] op_sel_hi:[1,0,0] neg_lo:[1,0,0] neg_hi:[1,0,0]
	v_mfma_f32_16x16x32_f16 v[22:25], v[10:13], v[2:5], 0
	ds_read2_b64 v[88:91], v32 offset0:10 offset1:212
	s_waitcnt lgkmcnt(11)
	v_pk_fma_f16 v2, v60, v6, v2
	v_pk_fma_f16 v3, v61, v7, v3
	v_pk_fma_f16 v4, v62, v8, v4
	v_pk_fma_f16 v5, v63, v9, v5
	v_cndmask_b32_e64 v28, v28, v20, s[60:61]
	v_pk_fma_f16 v6, v2, v128, v129 op_sel:[0,0,0] op_sel_hi:[1,0,0] neg_lo:[1,0,0] neg_hi:[1,0,0]
	v_pk_fma_f16 v7, v3, v128, v129 op_sel:[0,0,0] op_sel_hi:[1,0,0] neg_lo:[1,0,0] neg_hi:[1,0,0]
	v_pk_fma_f16 v8, v4, v128, v129 op_sel:[0,0,0] op_sel_hi:[1,0,0] neg_lo:[1,0,0] neg_hi:[1,0,0]
	v_pk_fma_f16 v9, v5, v128, v129 op_sel:[0,0,0] op_sel_hi:[1,0,0] neg_lo:[1,0,0] neg_hi:[1,0,0]
	v_mfma_f32_16x16x32_f16 v[18:21], v[10:13], v[2:5], 0
	ds_read2_b64 v[92:95], v32 offset0:11 offset1:213
	ds_read_b128 v[140:143], v33 offset:80
	v_pk_fma_f16 v2, v64, v6, v2
	v_pk_fma_f16 v3, v65, v7, v3
	v_pk_fma_f16 v4, v66, v8, v4
	v_pk_fma_f16 v5, v67, v9, v5
	v_cndmask_b32_e64 v29, v29, v25, s[60:61]
	v_pk_fma_f16 v6, v2, v130, v131 op_sel:[0,0,0] op_sel_hi:[1,0,0] neg_lo:[1,0,0] neg_hi:[1,0,0]
	v_pk_fma_f16 v7, v3, v130, v131 op_sel:[0,0,0] op_sel_hi:[1,0,0] neg_lo:[1,0,0] neg_hi:[1,0,0]
	v_pk_fma_f16 v8, v4, v130, v131 op_sel:[0,0,0] op_sel_hi:[1,0,0] neg_lo:[1,0,0] neg_hi:[1,0,0]
	v_pk_fma_f16 v9, v5, v130, v131 op_sel:[0,0,0] op_sel_hi:[1,0,0] neg_lo:[1,0,0] neg_hi:[1,0,0]
	v_mfma_f32_16x16x32_f16 v[22:25], v[10:13], v[2:5], 0
	ds_read2_b64 v[96:99], v32 offset0:12 offset1:214
	v_pk_fma_f16 v2, v68, v6, v2
	v_pk_fma_f16 v3, v69, v7, v3
	v_pk_fma_f16 v4, v70, v8, v4
	v_pk_fma_f16 v5, v71, v9, v5
	v_cndmask_b32_e64 v26, v26, v18, s[62:63]
	v_pk_fma_f16 v6, v2, v132, v133 op_sel:[0,0,0] op_sel_hi:[1,0,0] neg_lo:[1,0,0] neg_hi:[1,0,0]
	v_pk_fma_f16 v7, v3, v132, v133 op_sel:[0,0,0] op_sel_hi:[1,0,0] neg_lo:[1,0,0] neg_hi:[1,0,0]
	v_pk_fma_f16 v8, v4, v132, v133 op_sel:[0,0,0] op_sel_hi:[1,0,0] neg_lo:[1,0,0] neg_hi:[1,0,0]
	v_pk_fma_f16 v9, v5, v132, v133 op_sel:[0,0,0] op_sel_hi:[1,0,0] neg_lo:[1,0,0] neg_hi:[1,0,0]
	v_mfma_f32_16x16x32_f16 v[18:21], v[10:13], v[2:5], 0
	ds_read2_b64 v[100:103], v32 offset0:13 offset1:215
	ds_read_b128 v[144:147], v33 offset:96
	v_pk_fma_f16 v2, v72, v6, v2
	v_pk_fma_f16 v3, v73, v7, v3
	v_pk_fma_f16 v4, v74, v8, v4
	v_pk_fma_f16 v5, v75, v9, v5
	v_cndmask_b32_e64 v27, v27, v23, s[62:63]
	v_pk_fma_f16 v6, v2, v134, v135 op_sel:[0,0,0] op_sel_hi:[1,0,0] neg_lo:[1,0,0] neg_hi:[1,0,0]
	v_pk_fma_f16 v7, v3, v134, v135 op_sel:[0,0,0] op_sel_hi:[1,0,0] neg_lo:[1,0,0] neg_hi:[1,0,0]
	v_pk_fma_f16 v8, v4, v134, v135 op_sel:[0,0,0] op_sel_hi:[1,0,0] neg_lo:[1,0,0] neg_hi:[1,0,0]
	v_pk_fma_f16 v9, v5, v134, v135 op_sel:[0,0,0] op_sel_hi:[1,0,0] neg_lo:[1,0,0] neg_hi:[1,0,0]
	v_mfma_f32_16x16x32_f16 v[22:25], v[10:13], v[2:5], 0
	ds_read2_b64 v[104:107], v32 offset0:14 offset1:216
	s_waitcnt lgkmcnt(4)
	v_pk_fma_f16 v2, v76, v6, v2
	v_pk_fma_f16 v3, v77, v7, v3
	v_pk_fma_f16 v4, v78, v8, v4
	v_pk_fma_f16 v5, v79, v9, v5
	v_cndmask_b32_e64 v28, v28, v20, s[62:63]
	v_pk_fma_f16 v6, v2, v136, v137 op_sel:[0,0,0] op_sel_hi:[1,0,0] neg_lo:[1,0,0] neg_hi:[1,0,0]
	v_pk_fma_f16 v7, v3, v136, v137 op_sel:[0,0,0] op_sel_hi:[1,0,0] neg_lo:[1,0,0] neg_hi:[1,0,0]
	v_pk_fma_f16 v8, v4, v136, v137 op_sel:[0,0,0] op_sel_hi:[1,0,0] neg_lo:[1,0,0] neg_hi:[1,0,0]
	v_pk_fma_f16 v9, v5, v136, v137 op_sel:[0,0,0] op_sel_hi:[1,0,0] neg_lo:[1,0,0] neg_hi:[1,0,0]
	v_mfma_f32_16x16x32_f16 v[18:21], v[10:13], v[2:5], 0
	ds_read2_b64 v[108:111], v32 offset0:15 offset1:217
	ds_read_b128 v[148:151], v33 offset:112
	v_pk_fma_f16 v2, v80, v6, v2
	v_pk_fma_f16 v3, v81, v7, v3
	v_pk_fma_f16 v4, v82, v8, v4
	v_pk_fma_f16 v5, v83, v9, v5
	v_cndmask_b32_e64 v29, v29, v25, s[62:63]
	v_readfirstlane_b32 s4, v37
	v_readfirstlane_b32 s5, v38
	s_and_b32 s4, s4, s5
	s_cbranch_scc0 .Lc0_slow0
.Lc0_back0:
	v_pk_fma_f16 v6, v2, v138, v139 op_sel:[0,0,0] op_sel_hi:[1,0,0] neg_lo:[1,0,0] neg_hi:[1,0,0]
	v_pk_fma_f16 v7, v3, v138, v139 op_sel:[0,0,0] op_sel_hi:[1,0,0] neg_lo:[1,0,0] neg_hi:[1,0,0]
	v_pk_fma_f16 v8, v4, v138, v139 op_sel:[0,0,0] op_sel_hi:[1,0,0] neg_lo:[1,0,0] neg_hi:[1,0,0]
	v_pk_fma_f16 v9, v5, v138, v139 op_sel:[0,0,0] op_sel_hi:[1,0,0] neg_lo:[1,0,0] neg_hi:[1,0,0]
	v_mfma_f32_16x16x32_f16 v[22:25], v[10:13], v[2:5], 0
	ds_read2_b64 v[48:51], v32 offset0:16 offset1:218
	v_pk_fma_f16 v2, v84, v6, v2
	v_pk_fma_f16 v3, v85, v7, v3
	v_pk_fma_f16 v4, v86, v8, v4
	v_pk_fma_f16 v5, v87, v9, v5
	v_cndmask_b32_e64 v26, v26, v18, s[64:65]
	v_pk_fma_f16 v6, v2, v140, v141 op_sel:[0,0,0] op_sel_hi:[1,0,0] neg_lo:[1,0,0] neg_hi:[1,0,0]
	v_pk_fma_f16 v7, v3, v140, v141 op_sel:[0,0,0] op_sel_hi:[1,0,0] neg_lo:[1,0,0] neg_hi:[1,0,0]
	v_pk_fma_f16 v8, v4, v140, v141 op_sel:[0,0,0] op_sel_hi:[1,0,0] neg_lo:[1,0,0] neg_hi:[1,0,0]
	v_pk_fma_f16 v9, v5, v140, v141 op_sel:[0,0,0] op_sel_hi:[1,0,0] neg_lo:[1,0,0] neg_hi:[1,0,0]
	v_mfma_f32_16x16x32_f16 v[18:21], v[10:13], v[2:5], 0
	ds_read2_b64 v[52:55], v32 offset0:17 offset1:219
	ds_read_b128 v[120:123], v33 offset:128
	ds_read2_b64 v[14:17], v34 offset0:16 offset1:218
	v_pk_fma_f16 v2, v88, v6, v2
	v_pk_fma_f16 v3, v89, v7, v3
	v_pk_fma_f16 v4, v90, v8, v4
	v_pk_fma_f16 v5, v91, v9, v5
	v_cndmask_b32_e64 v27, v27, v23, s[64:65]
	v_pk_fma_f16 v6, v2, v142, v143 op_sel:[0,0,0] op_sel_hi:[1,0,0] neg_lo:[1,0,0] neg_hi:[1,0,0]
	v_pk_fma_f16 v7, v3, v142, v143 op_sel:[0,0,0] op_sel_hi:[1,0,0] neg_lo:[1,0,0] neg_hi:[1,0,0]
	v_pk_fma_f16 v8, v4, v142, v143 op_sel:[0,0,0] op_sel_hi:[1,0,0] neg_lo:[1,0,0] neg_hi:[1,0,0]
	v_pk_fma_f16 v9, v5, v142, v143 op_sel:[0,0,0] op_sel_hi:[1,0,0] neg_lo:[1,0,0] neg_hi:[1,0,0]
	v_mfma_f32_16x16x32_f16 v[22:25], v[10:13], v[2:5], 0
	ds_read2_b64 v[56:59], v32 offset0:18 offset1:220
	s_waitcnt lgkmcnt(5)
	v_pk_fma_f16 v2, v92, v6, v2
	v_pk_fma_f16 v3, v93, v7, v3
	v_pk_fma_f16 v4, v94, v8, v4
	v_pk_fma_f16 v5, v95, v9, v5
	v_cndmask_b32_e64 v28, v28, v20, s[64:65]
	v_pk_fma_f16 v6, v2, v144, v145 op_sel:[0,0,0] op_sel_hi:[1,0,0] neg_lo:[1,0,0] neg_hi:[1,0,0]
	v_pk_fma_f16 v7, v3, v144, v145 op_sel:[0,0,0] op_sel_hi:[1,0,0] neg_lo:[1,0,0] neg_hi:[1,0,0]
	v_pk_fma_f16 v8, v4, v144, v145 op_sel:[0,0,0] op_sel_hi:[1,0,0] neg_lo:[1,0,0] neg_hi:[1,0,0]
	v_pk_fma_f16 v9, v5, v144, v145 op_sel:[0,0,0] op_sel_hi:[1,0,0] neg_lo:[1,0,0] neg_hi:[1,0,0]
	v_mfma_f32_16x16x32_f16 v[18:21], v[10:13], v[2:5], 0
	ds_read2_b64 v[60:63], v32 offset0:19 offset1:221
	ds_read_b128 v[124:127], v33 offset:144
	v_pk_fma_f16 v2, v96, v6, v2
	v_pk_fma_f16 v3, v97, v7, v3
	v_pk_fma_f16 v4, v98, v8, v4
	v_pk_fma_f16 v5, v99, v9, v5
	v_cndmask_b32_e64 v29, v29, v25, s[64:65]
	v_pk_fma_f16 v6, v2, v146, v147 op_sel:[0,0,0] op_sel_hi:[1,0,0] neg_lo:[1,0,0] neg_hi:[1,0,0]
	v_pk_fma_f16 v7, v3, v146, v147 op_sel:[0,0,0] op_sel_hi:[1,0,0] neg_lo:[1,0,0] neg_hi:[1,0,0]
	v_pk_fma_f16 v8, v4, v146, v147 op_sel:[0,0,0] op_sel_hi:[1,0,0] neg_lo:[1,0,0] neg_hi:[1,0,0]
	v_pk_fma_f16 v9, v5, v146, v147 op_sel:[0,0,0] op_sel_hi:[1,0,0] neg_lo:[1,0,0] neg_hi:[1,0,0]
	v_mfma_f32_16x16x32_f16 v[22:25], v[10:13], v[2:5], 0
	ds_read2_b64 v[64:67], v32 offset0:20 offset1:222
	v_pk_fma_f16 v2, v100, v6, v2
	v_pk_fma_f16 v3, v101, v7, v3
	v_pk_fma_f16 v4, v102, v8, v4
	v_pk_fma_f16 v5, v103, v9, v5
	v_cndmask_b32_e64 v26, v26, v18, s[66:67]
	v_pk_fma_f16 v6, v2, v148, v149 op_sel:[0,0,0] op_sel_hi:[1,0,0] neg_lo:[1,0,0] neg_hi:[1,0,0]
	v_pk_fma_f16 v7, v3, v148, v149 op_sel:[0,0,0] op_sel_hi:[1,0,0] neg_lo:[1,0,0] neg_hi:[1,0,0]
	v_pk_fma_f16 v8, v4, v148, v149 op_sel:[0,0,0] op_sel_hi:[1,0,0] neg_lo:[1,0,0] neg_hi:[1,0,0]
	v_pk_fma_f16 v9, v5, v148, v149 op_sel:[0,0,0] op_sel_hi:[1,0,0] neg_lo:[1,0,0] neg_hi:[1,0,0]
	v_mfma_f32_16x16x32_f16 v[18:21], v[10:13], v[2:5], 0
	ds_read2_b64 v[68:71], v32 offset0:21 offset1:223
	ds_read_b128 v[128:131], v33 offset:160
	v_pk_fma_f16 v2, v104, v6, v2
	v_pk_fma_f16 v3, v105, v7, v3
	v_pk_fma_f16 v4, v106, v8, v4
	v_pk_fma_f16 v5, v107, v9, v5
	v_cndmask_b32_e64 v27, v27, v23, s[66:67]
	v_pk_fma_f16 v6, v2, v150, v151 op_sel:[0,0,0] op_sel_hi:[1,0,0] neg_lo:[1,0,0] neg_hi:[1,0,0]
	v_pk_fma_f16 v7, v3, v150, v151 op_sel:[0,0,0] op_sel_hi:[1,0,0] neg_lo:[1,0,0] neg_hi:[1,0,0]
	v_pk_fma_f16 v8, v4, v150, v151 op_sel:[0,0,0] op_sel_hi:[1,0,0] neg_lo:[1,0,0] neg_hi:[1,0,0]
	v_pk_fma_f16 v9, v5, v150, v151 op_sel:[0,0,0] op_sel_hi:[1,0,0] neg_lo:[1,0,0] neg_hi:[1,0,0]
	v_mfma_f32_16x16x32_f16 v[22:25], v[10:13], v[2:5], 0
	ds_read2_b64 v[72:75], v32 offset0:22 offset1:224
	s_waitcnt lgkmcnt(4)
	v_pk_fma_f16 v2, v108, v6, v2
	v_pk_fma_f16 v3, v109, v7, v3
	v_pk_fma_f16 v4, v110, v8, v4
	v_pk_fma_f16 v5, v111, v9, v5
	v_cndmask_b32_e64 v28, v28, v20, s[66:67]
.Lc0_next0:
	v_pk_fma_f16 v6, v2, v120, v121 op_sel:[0,0,0] op_sel_hi:[1,0,0] neg_lo:[1,0,0] neg_hi:[1,0,0]
	v_pk_fma_f16 v7, v3, v120, v121 op_sel:[0,0,0] op_sel_hi:[1,0,0] neg_lo:[1,0,0] neg_hi:[1,0,0]
	v_pk_fma_f16 v8, v4, v120, v121 op_sel:[0,0,0] op_sel_hi:[1,0,0] neg_lo:[1,0,0] neg_hi:[1,0,0]
	v_pk_fma_f16 v9, v5, v120, v121 op_sel:[0,0,0] op_sel_hi:[1,0,0] neg_lo:[1,0,0] neg_hi:[1,0,0]
	v_mfma_f32_16x16x32_f16 v[18:21], v[14:17], v[2:5], 0
	ds_read2_b64 v[76:79], v32 offset0:23 offset1:225
	ds_read_b128 v[132:135], v33 offset:176
	ds_read_b32 v37, v36 offset:8
	ds_read_b32 v38, v36 offset:72
	v_pk_fma_f16 v2, v48, v6, v2
	v_pk_fma_f16 v3, v49, v7, v3
	v_pk_fma_f16 v4, v50, v8, v4
	v_pk_fma_f16 v5, v51, v9, v5
	v_cndmask_b32_e64 v29, v29, v25, s[66:67]
	v_cvt_pk_f16_f32 v30, v26, v27
	v_cvt_pk_f16_f32 v31, v28, v29
	ds_write_b16 v39, v30 offset:2048
	ds_write_b16_d16_hi v39, v30 offset:2112
	ds_write_b16 v39, v31 offset:2176
	ds_write_b16_d16_hi v39, v31 offset:2240
	s_mov_b64 exec, 1
	ds_add_u32 v36, v44 offset:128
	s_mov_b64 exec, -1
	v_pk_fma_f16 v6, v2, v122, v123 op_sel:[0,0,0] op_sel_hi:[1,0,0] neg_lo:[1,0,0] neg_hi:[1,0,0]
	v_pk_fma_f16 v7, v3, v122, v123 op_sel:[0,0,0] op_sel_hi:[1,0,0] neg_lo:[1,0,0] neg_hi:[1,0,0]
	v_pk_fma_f16 v8, v4, v122, v123 op_sel:[0,0,0] op_sel_hi:[1,0,0] neg_lo:[1,0,0] neg_hi:[1,0,0]
	v_pk_fma_f16 v9, v5, v122, v123 op_sel:[0,0,0] op_sel_hi:[1,0,0] neg_lo:[1,0,0] neg_hi:[1,0,0]
	v_mfma_f32_16x16x32_f16 v[22:25], v[14:17], v[2:5], 0
	ds_read2_b64 v[80:83], v32 offset0:24 offset1:226
	v_pk_fma_f16 v2, v52, v6, v2
	v_pk_fma_f16 v3, v53, v7, v3
	v_pk_fma_f16 v4, v54, v8, v4
	v_pk_fma_f16 v5, v55, v9, v5
	v_cndmask_b32_e64 v26, v26, v18, s[60:61]
	v_pk_fma_f16 v6, v2, v124, v125 op_sel:[0,0,0] op_sel_hi:[1,0,0] neg_lo:[1,0,0] neg_hi:[1,0,0]
	v_pk_fma_f16 v7, v3, v124, v125 op_sel:[0,0,0] op_sel_hi:[1,0,0] neg_lo:[1,0,0] neg_hi:[1,0,0]
	v_pk_fma_f16 v8, v4, v124, v125 op_sel:[0,0,0] op_sel_hi:[1,0,0] neg_lo:[1,0,0] neg_hi:[1,0,0]
	v_pk_fma_f16 v9, v5, v124, v125 op_sel:[0,0,0] op_sel_hi:[1,0,0] neg_lo:[1,0,0] neg_hi:[1,0,0]
	v_mfma_f32_16x16x32_f16 v[18:21], v[14:17], v[2:5], 0
	ds_read2_b64 v[84:87], v32 offset0:25 offset1:227
	ds_read_b128 v[136:139], v33 offset:192
	v_pk_fma_f16 v2, v56, v6, v2
	v_pk_fma_f16 v3, v57, v7, v3
	v_pk_fma_f16 v4, v58, v8, v4
	v_pk_fma_f16 v5, v59, v9, v5
	v_cndmask_b32_e64 v27, v27, v23, s[60:61]
	v_pk_fma_f16 v6, v2, v126, v127 op_sel:[0,0,0] op_sel_hi:[1,0,0] neg_lo:[1,0,0] neg_hi:[1,0,0]
	v_pk_fma_f16 v7, v3, v126, v127 op_sel:[0,0,0] op_sel_hi:[1,0,0] neg_lo:[1,0,0] neg_hi:[1,0,0]
	v_pk_fma_f16 v8, v4, v126, v127 op_sel:[0,0,0] op_sel_hi:[1,0,0] neg_lo:[1,0,0] neg_hi:[1,0,0]
	v_pk_fma_f16 v9, v5, v126, v127 op_sel:[0,0,0] op_sel_hi:[1,0,0] neg_lo:[1,0,0] neg_hi:[1,0,0]
	v_mfma_f32_16x16x32_f16 v[22:25], v[14:17], v[2:5], 0
	ds_read2_b64 v[88:91], v32 offset0:26 offset1:228
	s_waitcnt lgkmcnt(11)
	v_pk_fma_f16 v2, v60, v6, v2
	v_pk_fma_f16 v3, v61, v7, v3
	v_pk_fma_f16 v4, v62, v8, v4
	v_pk_fma_f16 v5, v63, v9, v5
	v_cndmask_b32_e64 v28, v28, v20, s[60:61]
	v_pk_fma_f16 v6, v2, v128, v129 op_sel:[0,0,0] op_sel_hi:[1,0,0] neg_lo:[1,0,0] neg_hi:[1,0,0]
	v_pk_fma_f16 v7, v3, v128, v129 op_sel:[0,0,0] op_sel_hi:[1,0,0] neg_lo:[1,0,0] neg_hi:[1,0,0]
	v_pk_fma_f16 v8, v4, v128, v129 op_sel:[0,0,0] op_sel_hi:[1,0,0] neg_lo:[1,0,0] neg_hi:[1,0,0]
	v_pk_fma_f16 v9, v5, v128, v129 op_sel:[0,0,0] op_sel_hi:[1,0,0] neg_lo:[1,0,0] neg_hi:[1,0,0]
	v_mfma_f32_16x16x32_f16 v[18:21], v[14:17], v[2:5], 0
	ds_read2_b64 v[92:95], v32 offset0:27 offset1:229
	ds_read_b128 v[140:143], v33 offset:208
	v_pk_fma_f16 v2, v64, v6, v2
	v_pk_fma_f16 v3, v65, v7, v3
	v_pk_fma_f16 v4, v66, v8, v4
	v_pk_fma_f16 v5, v67, v9, v5
	v_cndmask_b32_e64 v29, v29, v25, s[60:61]
	v_pk_fma_f16 v6, v2, v130, v131 op_sel:[0,0,0] op_sel_hi:[1,0,0] neg_lo:[1,0,0] neg_hi:[1,0,0]
	v_pk_fma_f16 v7, v3, v130, v131 op_sel:[0,0,0] op_sel_hi:[1,0,0] neg_lo:[1,0,0] neg_hi:[1,0,0]
	v_pk_fma_f16 v8, v4, v130, v131 op_sel:[0,0,0] op_sel_hi:[1,0,0] neg_lo:[1,0,0] neg_hi:[1,0,0]
	v_pk_fma_f16 v9, v5, v130, v131 op_sel:[0,0,0] op_sel_hi:[1,0,0] neg_lo:[1,0,0] neg_hi:[1,0,0]
	v_mfma_f32_16x16x32_f16 v[22:25], v[14:17], v[2:5], 0
	ds_read2_b64 v[96:99], v32 offset0:28 offset1:230
	v_pk_fma_f16 v2, v68, v6, v2
	v_pk_fma_f16 v3, v69, v7, v3
	v_pk_fma_f16 v4, v70, v8, v4
	v_pk_fma_f16 v5, v71, v9, v5
	v_cndmask_b32_e64 v26, v26, v18, s[62:63]
	v_pk_fma_f16 v6, v2, v132, v133 op_sel:[0,0,0] op_sel_hi:[1,0,0] neg_lo:[1,0,0] neg_hi:[1,0,0]
	v_pk_fma_f16 v7, v3, v132, v133 op_sel:[0,0,0] op_sel_hi:[1,0,0] neg_lo:[1,0,0] neg_hi:[1,0,0]
	v_pk_fma_f16 v8, v4, v132, v133 op_sel:[0,0,0] op_sel_hi:[1,0,0] neg_lo:[1,0,0] neg_hi:[1,0,0]
	v_pk_fma_f16 v9, v5, v132, v133 op_sel:[0,0,0] op_sel_hi:[1,0,0] neg_lo:[1,0,0] neg_hi:[1,0,0]
	v_mfma_f32_16x16x32_f16 v[18:21], v[14:17], v[2:5], 0
	ds_read2_b64 v[100:103], v32 offset0:29 offset1:231
	ds_read_b128 v[144:147], v33 offset:224
	v_pk_fma_f16 v2, v72, v6, v2
	v_pk_fma_f16 v3, v73, v7, v3
	v_pk_fma_f16 v4, v74, v8, v4
	v_pk_fma_f16 v5, v75, v9, v5
	v_cndmask_b32_e64 v27, v27, v23, s[62:63]
	v_pk_fma_f16 v6, v2, v134, v135 op_sel:[0,0,0] op_sel_hi:[1,0,0] neg_lo:[1,0,0] neg_hi:[1,0,0]
	v_pk_fma_f16 v7, v3, v134, v135 op_sel:[0,0,0] op_sel_hi:[1,0,0] neg_lo:[1,0,0] neg_hi:[1,0,0]
	v_pk_fma_f16 v8, v4, v134, v135 op_sel:[0,0,0] op_sel_hi:[1,0,0] neg_lo:[1,0,0] neg_hi:[1,0,0]
	v_pk_fma_f16 v9, v5, v134, v135 op_sel:[0,0,0] op_sel_hi:[1,0,0] neg_lo:[1,0,0] neg_hi:[1,0,0]
	v_mfma_f32_16x16x32_f16 v[22:25], v[14:17], v[2:5], 0
	ds_read2_b64 v[104:107], v32 offset0:30 offset1:232
	s_waitcnt lgkmcnt(4)
	v_pk_fma_f16 v2, v76, v6, v2
	v_pk_fma_f16 v3, v77, v7, v3
	v_pk_fma_f16 v4, v78, v8, v4
	v_pk_fma_f16 v5, v79, v9, v5
	v_cndmask_b32_e64 v28, v28, v20, s[62:63]
	v_pk_fma_f16 v6, v2, v136, v137 op_sel:[0,0,0] op_sel_hi:[1,0,0] neg_lo:[1,0,0] neg_hi:[1,0,0]
	v_pk_fma_f16 v7, v3, v136, v137 op_sel:[0,0,0] op_sel_hi:[1,0,0] neg_lo:[1,0,0] neg_hi:[1,0,0]
	v_pk_fma_f16 v8, v4, v136, v137 op_sel:[0,0,0] op_sel_hi:[1,0,0] neg_lo:[1,0,0] neg_hi:[1,0,0]
	v_pk_fma_f16 v9, v5, v136, v137 op_sel:[0,0,0] op_sel_hi:[1,0,0] neg_lo:[1,0,0] neg_hi:[1,0,0]
	v_mfma_f32_16x16x32_f16 v[18:21], v[14:17], v[2:5], 0
	ds_read2_b64 v[108:111], v32 offset0:31 offset1:233
	ds_read_b128 v[148:151], v33 offset:240
	v_pk_fma_f16 v2, v80, v6, v2
	v_pk_fma_f16 v3, v81, v7, v3
	v_pk_fma_f16 v4, v82, v8, v4
	v_pk_fma_f16 v5, v83, v9, v5
	v_cndmask_b32_e64 v29, v29, v25, s[62:63]
	v_readfirstlane_b32 s4, v37
	v_readfirstlane_b32 s5, v38
	s_and_b32 s4, s4, s5
	s_cbranch_scc0 .Lc0_slow1
.Lc0_back1:
	v_pk_fma_f16 v6, v2, v138, v139 op_sel:[0,0,0] op_sel_hi:[1,0,0] neg_lo:[1,0,0] neg_hi:[1,0,0]
	v_pk_fma_f16 v7, v3, v138, v139 op_sel:[0,0,0] op_sel_hi:[1,0,0] neg_lo:[1,0,0] neg_hi:[1,0,0]
	v_pk_fma_f16 v8, v4, v138, v139 op_sel:[0,0,0] op_sel_hi:[1,0,0] neg_lo:[1,0,0] neg_hi:[1,0,0]
	v_pk_fma_f16 v9, v5, v138, v139 op_sel:[0,0,0] op_sel_hi:[1,0,0] neg_lo:[1,0,0] neg_hi:[1,0,0]
	v_mfma_f32_16x16x32_f16 v[22:25], v[14:17], v[2:5], 0
	ds_read2_b64 v[48:51], v32 offset0:32 offset1:234
	v_pk_fma_f16 v2, v84, v6, v2
	v_pk_fma_f16 v3, v85, v7, v3
	v_pk_fma_f16 v4, v86, v8, v4
	v_pk_fma_f16 v5, v87, v9, v5
	v_cndmask_b32_e64 v26, v26, v18, s[64:65]
	v_pk_fma_f16 v6, v2, v140, v141 op_sel:[0,0,0] op_sel_hi:[1,0,0] neg_lo:[1,0,0] neg_hi:[1,0,0]
	v_pk_fma_f16 v7, v3, v140, v141 op_sel:[0,0,0] op_sel_hi:[1,0,0] neg_lo:[1,0,0] neg_hi:[1,0,0]
	v_pk_fma_f16 v8, v4, v140, v141 op_sel:[0,0,0] op_sel_hi:[1,0,0] neg_lo:[1,0,0] neg_hi:[1,0,0]
	v_pk_fma_f16 v9, v5, v140, v141 op_sel:[0,0,0] op_sel_hi:[1,0,0] neg_lo:[1,0,0] neg_hi:[1,0,0]
	v_mfma_f32_16x16x32_f16 v[18:21], v[14:17], v[2:5], 0
	ds_read2_b64 v[52:55], v32 offset0:33 offset1:235
	ds_read_b128 v[120:123], v33 offset:256
	ds_read2_b64 v[10:13], v34 offset0:32 offset1:234
	v_pk_fma_f16 v2, v88, v6, v2
	v_pk_fma_f16 v3, v89, v7, v3
	v_pk_fma_f16 v4, v90, v8, v4
	v_pk_fma_f16 v5, v91, v9, v5
	v_cndmask_b32_e64 v27, v27, v23, s[64:65]
	v_pk_fma_f16 v6, v2, v142, v143 op_sel:[0,0,0] op_sel_hi:[1,0,0] neg_lo:[1,0,0] neg_hi:[1,0,0]
	v_pk_fma_f16 v7, v3, v142, v143 op_sel:[0,0,0] op_sel_hi:[1,0,0] neg_lo:[1,0,0] neg_hi:[1,0,0]
	v_pk_fma_f16 v8, v4, v142, v143 op_sel:[0,0,0] op_sel_hi:[1,0,0] neg_lo:[1,0,0] neg_hi:[1,0,0]
	v_pk_fma_f16 v9, v5, v142, v143 op_sel:[0,0,0] op_sel_hi:[1,0,0] neg_lo:[1,0,0] neg_hi:[1,0,0]
	v_mfma_f32_16x16x32_f16 v[22:25], v[14:17], v[2:5], 0
	ds_read2_b64 v[56:59], v32 offset0:34 offset1:236
	s_waitcnt lgkmcnt(5)
	v_pk_fma_f16 v2, v92, v6, v2
	v_pk_fma_f16 v3, v93, v7, v3
	v_pk_fma_f16 v4, v94, v8, v4
	v_pk_fma_f16 v5, v95, v9, v5
	v_cndmask_b32_e64 v28, v28, v20, s[64:65]
	v_pk_fma_f16 v6, v2, v144, v145 op_sel:[0,0,0] op_sel_hi:[1,0,0] neg_lo:[1,0,0] neg_hi:[1,0,0]
	v_pk_fma_f16 v7, v3, v144, v145 op_sel:[0,0,0] op_sel_hi:[1,0,0] neg_lo:[1,0,0] neg_hi:[1,0,0]
	v_pk_fma_f16 v8, v4, v144, v145 op_sel:[0,0,0] op_sel_hi:[1,0,0] neg_lo:[1,0,0] neg_hi:[1,0,0]
	v_pk_fma_f16 v9, v5, v144, v145 op_sel:[0,0,0] op_sel_hi:[1,0,0] neg_lo:[1,0,0] neg_hi:[1,0,0]
	v_mfma_f32_16x16x32_f16 v[18:21], v[14:17], v[2:5], 0
	ds_read2_b64 v[60:63], v32 offset0:35 offset1:237
	ds_read_b128 v[124:127], v33 offset:272
	v_pk_fma_f16 v2, v96, v6, v2
	v_pk_fma_f16 v3, v97, v7, v3
	v_pk_fma_f16 v4, v98, v8, v4
	v_pk_fma_f16 v5, v99, v9, v5
	v_cndmask_b32_e64 v29, v29, v25, s[64:65]
	v_pk_fma_f16 v6, v2, v146, v147 op_sel:[0,0,0] op_sel_hi:[1,0,0] neg_lo:[1,0,0] neg_hi:[1,0,0]
	v_pk_fma_f16 v7, v3, v146, v147 op_sel:[0,0,0] op_sel_hi:[1,0,0] neg_lo:[1,0,0] neg_hi:[1,0,0]
	v_pk_fma_f16 v8, v4, v146, v147 op_sel:[0,0,0] op_sel_hi:[1,0,0] neg_lo:[1,0,0] neg_hi:[1,0,0]
	v_pk_fma_f16 v9, v5, v146, v147 op_sel:[0,0,0] op_sel_hi:[1,0,0] neg_lo:[1,0,0] neg_hi:[1,0,0]
	v_mfma_f32_16x16x32_f16 v[22:25], v[14:17], v[2:5], 0
	ds_read2_b64 v[64:67], v32 offset0:36 offset1:238
	v_pk_fma_f16 v2, v100, v6, v2
	v_pk_fma_f16 v3, v101, v7, v3
	v_pk_fma_f16 v4, v102, v8, v4
	v_pk_fma_f16 v5, v103, v9, v5
	v_cndmask_b32_e64 v26, v26, v18, s[66:67]
	v_pk_fma_f16 v6, v2, v148, v149 op_sel:[0,0,0] op_sel_hi:[1,0,0] neg_lo:[1,0,0] neg_hi:[1,0,0]
	v_pk_fma_f16 v7, v3, v148, v149 op_sel:[0,0,0] op_sel_hi:[1,0,0] neg_lo:[1,0,0] neg_hi:[1,0,0]
	v_pk_fma_f16 v8, v4, v148, v149 op_sel:[0,0,0] op_sel_hi:[1,0,0] neg_lo:[1,0,0] neg_hi:[1,0,0]
	v_pk_fma_f16 v9, v5, v148, v149 op_sel:[0,0,0] op_sel_hi:[1,0,0] neg_lo:[1,0,0] neg_hi:[1,0,0]
	v_mfma_f32_16x16x32_f16 v[18:21], v[14:17], v[2:5], 0
	ds_read2_b64 v[68:71], v32 offset0:37 offset1:239
	ds_read_b128 v[128:131], v33 offset:288
	v_pk_fma_f16 v2, v104, v6, v2
	v_pk_fma_f16 v3, v105, v7, v3
	v_pk_fma_f16 v4, v106, v8, v4
	v_pk_fma_f16 v5, v107, v9, v5
	v_cndmask_b32_e64 v27, v27, v23, s[66:67]
	v_pk_fma_f16 v6, v2, v150, v151 op_sel:[0,0,0] op_sel_hi:[1,0,0] neg_lo:[1,0,0] neg_hi:[1,0,0]
	v_pk_fma_f16 v7, v3, v150, v151 op_sel:[0,0,0] op_sel_hi:[1,0,0] neg_lo:[1,0,0] neg_hi:[1,0,0]
	v_pk_fma_f16 v8, v4, v150, v151 op_sel:[0,0,0] op_sel_hi:[1,0,0] neg_lo:[1,0,0] neg_hi:[1,0,0]
	v_pk_fma_f16 v9, v5, v150, v151 op_sel:[0,0,0] op_sel_hi:[1,0,0] neg_lo:[1,0,0] neg_hi:[1,0,0]
	v_mfma_f32_16x16x32_f16 v[22:25], v[14:17], v[2:5], 0
	ds_read2_b64 v[72:75], v32 offset0:38 offset1:240
	s_waitcnt lgkmcnt(4)
	v_pk_fma_f16 v2, v108, v6, v2
	v_pk_fma_f16 v3, v109, v7, v3
	v_pk_fma_f16 v4, v110, v8, v4
	v_pk_fma_f16 v5, v111, v9, v5
	v_cndmask_b32_e64 v28, v28, v20, s[66:67]
.Lc0_next1:
	v_add_u32_e32 v32, 0x100, v32
	v_add_u32_e32 v33, 0x100, v33
	v_add_u32_e32 v34, 0x100, v34
	v_add_u32_e32 v36, 8, v36
	v_add_u32_e32 v39, 0x1000, v39
	v_add_u32_e32 v43, 0x1000, v43
	v_add_u32_e32 v35, 0x800, v35
	s_xor_b32 s71, s71, 2
	s_add_i32 s70, s70, 1
	s_cmp_lt_u32 s70, 6
	s_cbranch_scc1 .Lc0_loop
	v_pk_fma_f16 v6, v2, v120, v121 op_sel:[0,0,0] op_sel_hi:[1,0,0] neg_lo:[1,0,0] neg_hi:[1,0,0]
	v_pk_fma_f16 v7, v3, v120, v121 op_sel:[0,0,0] op_sel_hi:[1,0,0] neg_lo:[1,0,0] neg_hi:[1,0,0]
	v_pk_fma_f16 v8, v4, v120, v121 op_sel:[0,0,0] op_sel_hi:[1,0,0] neg_lo:[1,0,0] neg_hi:[1,0,0]
	v_pk_fma_f16 v9, v5, v120, v121 op_sel:[0,0,0] op_sel_hi:[1,0,0] neg_lo:[1,0,0] neg_hi:[1,0,0]
	v_mfma_f32_16x16x32_f16 v[18:21], v[10:13], v[2:5], 0
	ds_read2_b64 v[76:79], v32 offset0:7 offset1:209
	ds_read_b128 v[132:135], v33 offset:48
	v_pk_fma_f16 v2, v48, v6, v2
	v_pk_fma_f16 v3, v49, v7, v3
	v_pk_fma_f16 v4, v50, v8, v4
	v_pk_fma_f16 v5, v51, v9, v5
	v_cndmask_b32_e64 v29, v29, v25, s[66:67]
	v_cvt_pk_f16_f32 v30, v26, v27
	v_cvt_pk_f16_f32 v31, v28, v29
	ds_write_b16 v39, v30 offset:0
	ds_write_b16_d16_hi v39, v30 offset:64
	ds_write_b16 v39, v31 offset:128
	ds_write_b16_d16_hi v39, v31 offset:192
	s_mov_b64 exec, 1
	ds_add_u32 v36, v44 offset:124
	s_mov_b64 exec, -1
	v_pk_fma_f16 v6, v2, v122, v123 op_sel:[0,0,0] op_sel_hi:[1,0,0] neg_lo:[1,0,0] neg_hi:[1,0,0]
	v_pk_fma_f16 v7, v3, v122, v123 op_sel:[0,0,0] op_sel_hi:[1,0,0] neg_lo:[1,0,0] neg_hi:[1,0,0]
	v_pk_fma_f16 v8, v4, v122, v123 op_sel:[0,0,0] op_sel_hi:[1,0,0] neg_lo:[1,0,0] neg_hi:[1,0,0]
	v_pk_fma_f16 v9, v5, v122, v123 op_sel:[0,0,0] op_sel_hi:[1,0,0] neg_lo:[1,0,0] neg_hi:[1,0,0]
	v_mfma_f32_16x16x32_f16 v[22:25], v[10:13], v[2:5], 0
	v_pk_fma_f16 v2, v52, v6, v2
	v_pk_fma_f16 v3, v53, v7, v3
	v_pk_fma_f16 v4, v54, v8, v4
	v_pk_fma_f16 v5, v55, v9, v5
	v_cndmask_b32_e64 v26, v26, v18, s[60:61]
	v_pk_fma_f16 v6, v2, v124, v125 op_sel:[0,0,0] op_sel_hi:[1,0,0] neg_lo:[1,0,0] neg_hi:[1,0,0]
	v_pk_fma_f16 v7, v3, v124, v125 op_sel:[0,0,0] op_sel_hi:[1,0,0] neg_lo:[1,0,0] neg_hi:[1,0,0]
	v_pk_fma_f16 v8, v4, v124, v125 op_sel:[0,0,0] op_sel_hi:[1,0,0] neg_lo:[1,0,0] neg_hi:[1,0,0]
	v_pk_fma_f16 v9, v5, v124, v125 op_sel:[0,0,0] op_sel_hi:[1,0,0] neg_lo:[1,0,0] neg_hi:[1,0,0]
	v_mfma_f32_16x16x32_f16 v[18:21], v[10:13], v[2:5], 0
	v_pk_fma_f16 v2, v56, v6, v2
	v_pk_fma_f16 v3, v57, v7, v3
	v_pk_fma_f16 v4, v58, v8, v4
	v_pk_fma_f16 v5, v59, v9, v5
	v_cndmask_b32_e64 v27, v27, v23, s[60:61]
	v_pk_fma_f16 v6, v2, v126, v127 op_sel:[0,0,0] op_sel_hi:[1,0,0] neg_lo:[1,0,0] neg_hi:[1,0,0]
	v_pk_fma_f16 v7, v3, v126, v127 op_sel:[0,0,0] op_sel_hi:[1,0,0] neg_lo:[1,0,0] neg_hi:[1,0,0]
	v_pk_fma_f16 v8, v4, v126, v127 op_sel:[0,0,0] op_sel_hi:[1,0,0] neg_lo:[1,0,0] neg_hi:[1,0,0]
	v_pk_fma_f16 v9, v5, v126, v127 op_sel:[0,0,0] op_sel_hi:[1,0,0] neg_lo:[1,0,0] neg_hi:[1,0,0]
	v_mfma_f32_16x16x32_f16 v[22:25], v[10:13], v[2:5], 0
	s_waitcnt lgkmcnt(5)
	v_pk_fma_f16 v2, v60, v6, v2
	v_pk_fma_f16 v3, v61, v7, v3
	v_pk_fma_f16 v4, v62, v8, v4
	v_pk_fma_f16 v5, v63, v9, v5
	v_cndmask_b32_e64 v28, v28, v20, s[60:61]
	v_pk_fma_f16 v6, v2, v128, v129 op_sel:[0,0,0] op_sel_hi:[1,0,0] neg_lo:[1,0,0] neg_hi:[1,0,0]
	v_pk_fma_f16 v7, v3, v128, v129 op_sel:[0,0,0] op_sel_hi:[1,0,0] neg_lo:[1,0,0] neg_hi:[1,0,0]
	v_pk_fma_f16 v8, v4, v128, v129 op_sel:[0,0,0] op_sel_hi:[1,0,0] neg_lo:[1,0,0] neg_hi:[1,0,0]
	v_pk_fma_f16 v9, v5, v128, v129 op_sel:[0,0,0] op_sel_hi:[1,0,0] neg_lo:[1,0,0] neg_hi:[1,0,0]
	v_mfma_f32_16x16x32_f16 v[18:21], v[10:13], v[2:5], 0
	v_pk_fma_f16 v2, v64, v6, v2
	v_pk_fma_f16 v3, v65, v7, v3
	v_pk_fma_f16 v4, v66, v8, v4
	v_pk_fma_f16 v5, v67, v9, v5
	v_cndmask_b32_e64 v29, v29, v25, s[60:61]
	v_pk_fma_f16 v6, v2, v130, v131 op_sel:[0,0,0] op_sel_hi:[1,0,0] neg_lo:[1,0,0] neg_hi:[1,0,0]
	v_pk_fma_f16 v7, v3, v130, v131 op_sel:[0,0,0] op_sel_hi:[1,0,0] neg_lo:[1,0,0] neg_hi:[1,0,0]
	v_pk_fma_f16 v8, v4, v130, v131 op_sel:[0,0,0] op_sel_hi:[1,0,0] neg_lo:[1,0,0] neg_hi:[1,0,0]
	v_pk_fma_f16 v9, v5, v130, v131 op_sel:[0,0,0] op_sel_hi:[1,0,0] neg_lo:[1,0,0] neg_hi:[1,0,0]
	v_mfma_f32_16x16x32_f16 v[22:25], v[10:13], v[2:5], 0
	v_pk_fma_f16 v2, v68, v6, v2
	v_pk_fma_f16 v3, v69, v7, v3
	v_pk_fma_f16 v4, v70, v8, v4
	v_pk_fma_f16 v5, v71, v9, v5
	v_cndmask_b32_e64 v26, v26, v18, s[62:63]
	v_pk_fma_f16 v6, v2, v132, v133 op_sel:[0,0,0] op_sel_hi:[1,0,0] neg_lo:[1,0,0] neg_hi:[1,0,0]
	v_pk_fma_f16 v7, v3, v132, v133 op_sel:[0,0,0] op_sel_hi:[1,0,0] neg_lo:[1,0,0] neg_hi:[1,0,0]
	v_pk_fma_f16 v8, v4, v132, v133 op_sel:[0,0,0] op_sel_hi:[1,0,0] neg_lo:[1,0,0] neg_hi:[1,0,0]
	v_pk_fma_f16 v9, v5, v132, v133 op_sel:[0,0,0] op_sel_hi:[1,0,0] neg_lo:[1,0,0] neg_hi:[1,0,0]
	v_mfma_f32_16x16x32_f16 v[18:21], v[10:13], v[2:5], 0
	v_pk_fma_f16 v2, v72, v6, v2
	v_pk_fma_f16 v3, v73, v7, v3
	v_pk_fma_f16 v4, v74, v8, v4
	v_pk_fma_f16 v5, v75, v9, v5
	v_cndmask_b32_e64 v27, v27, v23, s[62:63]
	v_pk_fma_f16 v6, v2, v134, v135 op_sel:[0,0,0] op_sel_hi:[1,0,0] neg_lo:[1,0,0] neg_hi:[1,0,0]
	v_pk_fma_f16 v7, v3, v134, v135 op_sel:[0,0,0] op_sel_hi:[1,0,0] neg_lo:[1,0,0] neg_hi:[1,0,0]
	v_pk_fma_f16 v8, v4, v134, v135 op_sel:[0,0,0] op_sel_hi:[1,0,0] neg_lo:[1,0,0] neg_hi:[1,0,0]
	v_pk_fma_f16 v9, v5, v134, v135 op_sel:[0,0,0] op_sel_hi:[1,0,0] neg_lo:[1,0,0] neg_hi:[1,0,0]
	v_mfma_f32_16x16x32_f16 v[22:25], v[10:13], v[2:5], 0
	v_pk_fma_f16 v2, v76, v6, v2
	v_pk_fma_f16 v3, v77, v7, v3
	v_pk_fma_f16 v4, v78, v8, v4
	v_pk_fma_f16 v5, v79, v9, v5
	v_cndmask_b32_e64 v28, v28, v20, s[62:63]
	s_nop 7
	v_cndmask_b32_e64 v29, v29, v25, s[62:63]
	v_cvt_pk_f16_f32 v30, v26, v27
	v_cvt_pk_f16_f32 v31, v28, v29
	ds_write_b16 v39, v30 offset:2048
	ds_write_b16_d16_hi v39, v30 offset:2112
	ds_write_b16 v39, v31 offset:2176
	ds_write_b16_d16_hi v39, v31 offset:2240
	s_mov_b64 exec, 1
	ds_add_u32 v36, v44 offset:128
	s_mov_b64 exec, -1
	s_branch .Lc0_end

.Lc_par1:
	ds_read2_b64 v[48:51], v32 offset0:0 offset1:202
	ds_read2_b64 v[52:55], v32 offset0:1 offset1:203
	ds_read_b128 v[120:123], v33 offset:0
	ds_read2_b64 v[10:13], v34 offset0:0 offset1:202
	ds_read2_b64 v[56:59], v32 offset0:2 offset1:204
	ds_read2_b64 v[60:63], v32 offset0:3 offset1:205
	ds_read_b128 v[124:127], v33 offset:16
	ds_read2_b64 v[64:67], v32 offset0:4 offset1:206
	ds_read2_b64 v[68:71], v32 offset0:5 offset1:207
	ds_read_b128 v[128:131], v33 offset:32
	ds_read2_b64 v[72:75], v32 offset0:6 offset1:208
	s_mov_b32 s70, 0
	s_mov_b32 s71, 0
	s_waitcnt lgkmcnt(4)
.Lc1_loop:
	v_pk_fma_f16 v6, v2, v120, v121 op_sel:[0,1,1] op_sel_hi:[1,1,1] neg_lo:[1,0,0] neg_hi:[1,0,0]
	v_pk_fma_f16 v7, v3, v120, v121 op_sel:[0,1,1] op_sel_hi:[1,1,1] neg_lo:[1,0,0] neg_hi:[1,0,0]
	v_pk_fma_f16 v8, v4, v120, v121 op_sel:[0,1,1] op_sel_hi:[1,1,1] neg_lo:[1,0,0] neg_hi:[1,0,0]
	v_pk_fma_f16 v9, v5, v120, v121 op_sel:[0,1,1] op_sel_hi:[1,1,1] neg_lo:[1,0,0] neg_hi:[1,0,0]
	v_mfma_f32_16x16x32_f16 v[18:21], v[10:13], v[2:5], 0
	ds_read2_b64 v[76:79], v32 offset0:7 offset1:209
	ds_read_b128 v[132:135], v33 offset:48
	ds_read_b32 v37, v36 offset:4
	ds_read_b32 v38, v36 offset:68
	v_pk_fma_f16 v2, v48, v6, v2
	v_pk_fma_f16 v3, v49, v7, v3
	v_pk_fma_f16 v4, v50, v8, v4
	v_pk_fma_f16 v5, v51, v9, v5
	v_cndmask_b32_e64 v29, v29, v25, s[66:67]
	v_cvt_pk_f16_f32 v30, v26, v27
	v_cvt_pk_f16_f32 v31, v28, v29
	ds_write_b16 v39, v30 offset:0
	ds_write_b16_d16_hi v39, v30 offset:64
	ds_write_b16 v39, v31 offset:128
	ds_write_b16_d16_hi v39, v31 offset:192
	s_mov_b64 exec, 1
	ds_add_u32 v36, v44 offset:124
	s_mov_b64 exec, -1
	v_pk_fma_f16 v6, v2, v122, v123 op_sel:[0,1,1] op_sel_hi:[1,1,1] neg_lo:[1,0,0] neg_hi:[1,0,0]
	v_pk_fma_f16 v7, v3, v122, v123 op_sel:[0,1,1] op_sel_hi:[1,1,1] neg_lo:[1,0,0] neg_hi:[1,0,0]
	v_pk_fma_f16 v8, v4, v122, v123 op_sel:[0,1,1] op_sel_hi:[1,1,1] neg_lo:[1,0,0] neg_hi:[1,0,0]
	v_pk_fma_f16 v9, v5, v122, v123 op_sel:[0,1,1] op_sel_hi:[1,1,1] neg_lo:[1,0,0] neg_hi:[1,0,0]
	v_mfma_f32_16x16x32_f16 v[22:25], v[10:13], v[2:5], 0
	ds_read2_b64 v[80:83], v32 offset0:8 offset1:210
	v_pk_fma_f16 v2, v52, v6, v2
	v_pk_fma_f16 v3, v53, v7, v3
	v_pk_fma_f16 v4, v54, v8, v4
	v_pk_fma_f16 v5, v55, v9, v5
	v_cndmask_b32_e64 v26, v26, v18, s[60:61]
	v_pk_fma_f16 v6, v2, v124, v125 op_sel:[0,1,1] op_sel_hi:[1,1,1] neg_lo:[1,0,0] neg_hi:[1,0,0]
	v_pk_fma_f16 v7, v3, v124, v125 op_sel:[0,1,1] op_sel_hi:[1,1,1] neg_lo:[1,0,0] neg_hi:[1,0,0]
	v_pk_fma_f16 v8, v4, v124, v125 op_sel:[0,1,1] op_sel_hi:[1,1,1] neg_lo:[1,0,0] neg_hi:[1,0,0]
	v_pk_fma_f16 v9, v5, v124, v125 op_sel:[0,1,1] op_sel_hi:[1,1,1] neg_lo:[1,0,0] neg_hi:[1,0,0]
	v_mfma_f32_16x16x32_f16 v[18:21], v[10:13], v[2:5], 0
	ds_read2_b64 v[84:87], v32 offset0:9 offset1:211
	ds_read_b128 v[136:139], v33 offset:64
	v_pk_fma_f16 v2, v56, v6, v2
	v_pk_fma_f16 v3, v57, v7, v3
	v_pk_fma_f16 v4, v58, v8, v4
	v_pk_fma_f16 v5, v59, v9, v5
	v_cndmask_b32_e64 v27, v27, v23, s[60:61]
	v_pk_fma_f16 v6, v2, v126, v127 op_sel:[0,1,1] op_sel_hi:[1,1,1] neg_lo:[1,0,0] neg_hi:[1,0,0]
	v_pk_fma_f16 v7, v3, v126, v127 op_sel:[0,1,1] op_sel_hi:[1,1,1] neg_lo:[1,0,0] neg_hi:[1,0,0]
	v_pk_fma_f16 v8, v4, v126, v127 op_sel:[0,1,1] op_sel_hi:[1,1,1] neg_lo:[1,0,0] neg_hi:[1,0,0]
	v_pk_fma_f16 v9, v5, v126, v127 op_sel:[0,1,1] op_sel_hi:[1,1,1] neg_lo:[1,0,0] neg_hi:[1,0,0]
	v_mfma_f32_16x16x32_f16 v[22:25], v[10:13], v[2:5], 0
	ds_read2_b64 v[88:91], v32 offset0:10 offset1:212
	s_waitcnt lgkmcnt(11)
	v_pk_fma_f16 v2, v60, v6, v2
	v_pk_fma_f16 v3, v61, v7, v3
	v_pk_fma_f16 v4, v62, v8, v4
	v_pk_fma_f16 v5, v63, v9, v5
	v_cndmask_b32_e64 v28, v28, v20, s[60:61]
	v_pk_fma_f16 v6, v2, v128, v129 op_sel:[0,1,1] op_sel_hi:[1,1,1] neg_lo:[1,0,0] neg_hi:[1,0,0]
	v_pk_fma_f16 v7, v3, v128, v129 op_sel:[0,1,1] op_sel_hi:[1,1,1] neg_lo:[1,0,0] neg_hi:[1,0,0]
	v_pk_fma_f16 v8, v4, v128, v129 op_sel:[0,1,1] op_sel_hi:[1,1,1] neg_lo:[1,0,0] neg_hi:[1,0,0]
	v_pk_fma_f16 v9, v5, v128, v129 op_sel:[0,1,1] op_sel_hi:[1,1,1] neg_lo:[1,0,0] neg_hi:[1,0,0]
	v_mfma_f32_16x16x32_f16 v[18:21], v[10:13], v[2:5], 0
	ds_read2_b64 v[92:95], v32 offset0:11 offset1:213
	ds_read_b128 v[140:143], v33 offset:80
	v_pk_fma_f16 v2, v64, v6, v2
	v_pk_fma_f16 v3, v65, v7, v3
	v_pk_fma_f16 v4, v66, v8, v4
	v_pk_fma_f16 v5, v67, v9, v5
	v_cndmask_b32_e64 v29, v29, v25, s[60:61]
	v_pk_fma_f16 v6, v2, v130, v131 op_sel:[0,1,1] op_sel_hi:[1,1,1] neg_lo:[1,0,0] neg_hi:[1,0,0]
	v_pk_fma_f16 v7, v3, v130, v131 op_sel:[0,1,1] op_sel_hi:[1,1,1] neg_lo:[1,0,0] neg_hi:[1,0,0]
	v_pk_fma_f16 v8, v4, v130, v131 op_sel:[0,1,1] op_sel_hi:[1,1,1] neg_lo:[1,0,0] neg_hi:[1,0,0]
	v_pk_fma_f16 v9, v5, v130, v131 op_sel:[0,1,1] op_sel_hi:[1,1,1] neg_lo:[1,0,0] neg_hi:[1,0,0]
	v_mfma_f32_16x16x32_f16 v[22:25], v[10:13], v[2:5], 0
	ds_read2_b64 v[96:99], v32 offset0:12 offset1:214
	v_pk_fma_f16 v2, v68, v6, v2
	v_pk_fma_f16 v3, v69, v7, v3
	v_pk_fma_f16 v4, v70, v8, v4
	v_pk_fma_f16 v5, v71, v9, v5
	v_cndmask_b32_e64 v26, v26, v18, s[62:63]
	v_pk_fma_f16 v6, v2, v132, v133 op_sel:[0,1,1] op_sel_hi:[1,1,1] neg_lo:[1,0,0] neg_hi:[1,0,0]
	v_pk_fma_f16 v7, v3, v132, v133 op_sel:[0,1,1] op_sel_hi:[1,1,1] neg_lo:[1,0,0] neg_hi:[1,0,0]
	v_pk_fma_f16 v8, v4, v132, v133 op_sel:[0,1,1] op_sel_hi:[1,1,1] neg_lo:[1,0,0] neg_hi:[1,0,0]
	v_pk_fma_f16 v9, v5, v132, v133 op_sel:[0,1,1] op_sel_hi:[1,1,1] neg_lo:[1,0,0] neg_hi:[1,0,0]
	v_mfma_f32_16x16x32_f16 v[18:21], v[10:13], v[2:5], 0
	ds_read2_b64 v[100:103], v32 offset0:13 offset1:215
	ds_read_b128 v[144:147], v33 offset:96
	v_pk_fma_f16 v2, v72, v6, v2
	v_pk_fma_f16 v3, v73, v7, v3
	v_pk_fma_f16 v4, v74, v8, v4
	v_pk_fma_f16 v5, v75, v9, v5
	v_cndmask_b32_e64 v27, v27, v23, s[62:63]
	v_pk_fma_f16 v6, v2, v134, v135 op_sel:[0,1,1] op_sel_hi:[1,1,1] neg_lo:[1,0,0] neg_hi:[1,0,0]
	v_pk_fma_f16 v7, v3, v134, v135 op_sel:[0,1,1] op_sel_hi:[1,1,1] neg_lo:[1,0,0] neg_hi:[1,0,0]
	v_pk_fma_f16 v8, v4, v134, v135 op_sel:[0,1,1] op_sel_hi:[1,1,1] neg_lo:[1,0,0] neg_hi:[1,0,0]
	v_pk_fma_f16 v9, v5, v134, v135 op_sel:[0,1,1] op_sel_hi:[1,1,1] neg_lo:[1,0,0] neg_hi:[1,0,0]
	v_mfma_f32_16x16x32_f16 v[22:25], v[10:13], v[2:5], 0
	ds_read2_b64 v[104:107], v32 offset0:14 offset1:216
	s_waitcnt lgkmcnt(4)
	v_pk_fma_f16 v2, v76, v6, v2
	v_pk_fma_f16 v3, v77, v7, v3
	v_pk_fma_f16 v4, v78, v8, v4
	v_pk_fma_f16 v5, v79, v9, v5
	v_cndmask_b32_e64 v28, v28, v20, s[62:63]
	v_pk_fma_f16 v6, v2, v136, v137 op_sel:[0,1,1] op_sel_hi:[1,1,1] neg_lo:[1,0,0] neg_hi:[1,0,0]
	v_pk_fma_f16 v7, v3, v136, v137 op_sel:[0,1,1] op_sel_hi:[1,1,1] neg_lo:[1,0,0] neg_hi:[1,0,0]
	v_pk_fma_f16 v8, v4, v136, v137 op_sel:[0,1,1] op_sel_hi:[1,1,1] neg_lo:[1,0,0] neg_hi:[1,0,0]
	v_pk_fma_f16 v9, v5, v136, v137 op_sel:[0,1,1] op_sel_hi:[1,1,1] neg_lo:[1,0,0] neg_hi:[1,0,0]
	v_mfma_f32_16x16x32_f16 v[18:21], v[10:13], v[2:5], 0
	ds_read2_b64 v[108:111], v32 offset0:15 offset1:217
	ds_read_b128 v[148:151], v33 offset:112
	v_pk_fma_f16 v2, v80, v6, v2
	v_pk_fma_f16 v3, v81, v7, v3
	v_pk_fma_f16 v4, v82, v8, v4
	v_pk_fma_f16 v5, v83, v9, v5
	v_cndmask_b32_e64 v29, v29, v25, s[62:63]
	v_readfirstlane_b32 s4, v37
	v_readfirstlane_b32 s5, v38
	s_and_b32 s4, s4, s5
	s_cbranch_scc0 .Lc1_slow0

.Lc1_nd0:
	v_pk_fma_f16 v6, v2, v138, v139 op_sel:[0,1,1] op_sel_hi:[1,1,1] neg_lo:[1,0,0] neg_hi:[1,0,0]
	v_pk_fma_f16 v7, v3, v138, v139 op_sel:[0,1,1] op_sel_hi:[1,1,1] neg_lo:[1,0,0] neg_hi:[1,0,0]
	v_pk_fma_f16 v8, v4, v138, v139 op_sel:[0,1,1] op_sel_hi:[1,1,1] neg_lo:[1,0,0] neg_hi:[1,0,0]
	v_pk_fma_f16 v9, v5, v138, v139 op_sel:[0,1,1] op_sel_hi:[1,1,1] neg_lo:[1,0,0] neg_hi:[1,0,0]
	v_mfma_f32_16x16x32_f16 v[22:25], v[10:13], v[2:5], 0
	ds_read2_b64 v[48:51], v32 offset0:16 offset1:218
	v_pk_fma_f16 v2, v84, v6, v2
	v_pk_fma_f16 v3, v85, v7, v3
	v_pk_fma_f16 v4, v86, v8, v4
	v_pk_fma_f16 v5, v87, v9, v5
	v_cndmask_b32_e64 v26, v26, v18, s[64:65]
	v_pk_fma_f16 v6, v2, v140, v141 op_sel:[0,1,1] op_sel_hi:[1,1,1] neg_lo:[1,0,0] neg_hi:[1,0,0]
	v_pk_fma_f16 v7, v3, v140, v141 op_sel:[0,1,1] op_sel_hi:[1,1,1] neg_lo:[1,0,0] neg_hi:[1,0,0]
	v_pk_fma_f16 v8, v4, v140, v141 op_sel:[0,1,1] op_sel_hi:[1,1,1] neg_lo:[1,0,0] neg_hi:[1,0,0]
	v_pk_fma_f16 v9, v5, v140, v141 op_sel:[0,1,1] op_sel_hi:[1,1,1] neg_lo:[1,0,0] neg_hi:[1,0,0]
	v_mfma_f32_16x16x32_f16 v[18:21], v[10:13], v[2:5], 0
	ds_read2_b64 v[52:55], v32 offset0:17 offset1:219
	ds_read_b128 v[120:123], v33 offset:128
	ds_read2_b64 v[14:17], v34 offset0:16 offset1:218
	v_pk_fma_f16 v2, v88, v6, v2
	v_pk_fma_f16 v3, v89, v7, v3
	v_pk_fma_f16 v4, v90, v8, v4
	v_pk_fma_f16 v5, v91, v9, v5
	v_cndmask_b32_e64 v27, v27, v23, s[64:65]
	v_pk_fma_f16 v6, v2, v142, v143 op_sel:[0,1,1] op_sel_hi:[1,1,1] neg_lo:[1,0,0] neg_hi:[1,0,0]
	v_pk_fma_f16 v7, v3, v142, v143 op_sel:[0,1,1] op_sel_hi:[1,1,1] neg_lo:[1,0,0] neg_hi:[1,0,0]
	v_pk_fma_f16 v8, v4, v142, v143 op_sel:[0,1,1] op_sel_hi:[1,1,1] neg_lo:[1,0,0] neg_hi:[1,0,0]
	v_pk_fma_f16 v9, v5, v142, v143 op_sel:[0,1,1] op_sel_hi:[1,1,1] neg_lo:[1,0,0] neg_hi:[1,0,0]
	v_mfma_f32_16x16x32_f16 v[22:25], v[10:13], v[2:5], 0
	ds_read2_b64 v[56:59], v32 offset0:18 offset1:220
	s_waitcnt lgkmcnt(5)
	v_pk_fma_f16 v2, v92, v6, v2
	v_pk_fma_f16 v3, v93, v7, v3
	v_pk_fma_f16 v4, v94, v8, v4
	v_pk_fma_f16 v5, v95, v9, v5
	v_cndmask_b32_e64 v28, v28, v20, s[64:65]
	v_pk_fma_f16 v6, v2, v144, v145 op_sel:[0,1,1] op_sel_hi:[1,1,1] neg_lo:[1,0,0] neg_hi:[1,0,0]
	v_pk_fma_f16 v7, v3, v144, v145 op_sel:[0,1,1] op_sel_hi:[1,1,1] neg_lo:[1,0,0] neg_hi:[1,0,0]
	v_pk_fma_f16 v8, v4, v144, v145 op_sel:[0,1,1] op_sel_hi:[1,1,1] neg_lo:[1,0,0] neg_hi:[1,0,0]
	v_pk_fma_f16 v9, v5, v144, v145 op_sel:[0,1,1] op_sel_hi:[1,1,1] neg_lo:[1,0,0] neg_hi:[1,0,0]
	v_mfma_f32_16x16x32_f16 v[18:21], v[10:13], v[2:5], 0
	ds_read2_b64 v[60:63], v32 offset0:19 offset1:221
	ds_read_b128 v[124:127], v33 offset:144
	v_pk_fma_f16 v2, v96, v6, v2
	v_pk_fma_f16 v3, v97, v7, v3
	v_pk_fma_f16 v4, v98, v8, v4
	v_pk_fma_f16 v5, v99, v9, v5
	v_cndmask_b32_e64 v29, v29, v25, s[64:65]
	s_cmp_eq_u32 s72, 1
	s_cbranch_scc0 .Lc1_ns0
	s_waitcnt lgkmcnt(7)
	v_readfirstlane_b32 s4, v45
	s_cmp_eq_u32 s4, 4
	s_cbranch_scc0 .Lc1_dslow0

.Lc1_ns0:
	v_pk_fma_f16 v6, v2, v146, v147 op_sel:[0,1,1] op_sel_hi:[1,1,1] neg_lo:[1,0,0] neg_hi:[1,0,0]
	v_pk_fma_f16 v7, v3, v146, v147 op_sel:[0,1,1] op_sel_hi:[1,1,1] neg_lo:[1,0,0] neg_hi:[1,0,0]
	v_pk_fma_f16 v8, v4, v146, v147 op_sel:[0,1,1] op_sel_hi:[1,1,1] neg_lo:[1,0,0] neg_hi:[1,0,0]
	v_pk_fma_f16 v9, v5, v146, v147 op_sel:[0,1,1] op_sel_hi:[1,1,1] neg_lo:[1,0,0] neg_hi:[1,0,0]
	v_mfma_f32_16x16x32_f16 v[22:25], v[10:13], v[2:5], 0
	ds_read2_b64 v[64:67], v32 offset0:20 offset1:222
	v_pk_fma_f16 v2, v100, v6, v2
	v_pk_fma_f16 v3, v101, v7, v3
	v_pk_fma_f16 v4, v102, v8, v4
	v_pk_fma_f16 v5, v103, v9, v5
	v_cndmask_b32_e64 v26, v26, v18, s[66:67]
	v_pk_fma_f16 v6, v2, v148, v149 op_sel:[0,1,1] op_sel_hi:[1,1,1] neg_lo:[1,0,0] neg_hi:[1,0,0]
	v_pk_fma_f16 v7, v3, v148, v149 op_sel:[0,1,1] op_sel_hi:[1,1,1] neg_lo:[1,0,0] neg_hi:[1,0,0]
	v_pk_fma_f16 v8, v4, v148, v149 op_sel:[0,1,1] op_sel_hi:[1,1,1] neg_lo:[1,0,0] neg_hi:[1,0,0]
	v_pk_fma_f16 v9, v5, v148, v149 op_sel:[0,1,1] op_sel_hi:[1,1,1] neg_lo:[1,0,0] neg_hi:[1,0,0]
	v_mfma_f32_16x16x32_f16 v[18:21], v[10:13], v[2:5], 0
	ds_read2_b64 v[68:71], v32 offset0:21 offset1:223
	ds_read_b128 v[128:131], v33 offset:160
	v_pk_fma_f16 v2, v104, v6, v2
	v_pk_fma_f16 v3, v105, v7, v3
	v_pk_fma_f16 v4, v106, v8, v4
	v_pk_fma_f16 v5, v107, v9, v5
	v_cndmask_b32_e64 v27, v27, v23, s[66:67]
	v_pk_fma_f16 v6, v2, v150, v151 op_sel:[0,1,1] op_sel_hi:[1,1,1] neg_lo:[1,0,0] neg_hi:[1,0,0]
	v_pk_fma_f16 v7, v3, v150, v151 op_sel:[0,1,1] op_sel_hi:[1,1,1] neg_lo:[1,0,0] neg_hi:[1,0,0]
	v_pk_fma_f16 v8, v4, v150, v151 op_sel:[0,1,1] op_sel_hi:[1,1,1] neg_lo:[1,0,0] neg_hi:[1,0,0]
	v_pk_fma_f16 v9, v5, v150, v151 op_sel:[0,1,1] op_sel_hi:[1,1,1] neg_lo:[1,0,0] neg_hi:[1,0,0]
	v_mfma_f32_16x16x32_f16 v[22:25], v[10:13], v[2:5], 0
	ds_read2_b64 v[72:75], v32 offset0:22 offset1:224
	s_waitcnt lgkmcnt(4)
	v_pk_fma_f16 v2, v108, v6, v2
	v_pk_fma_f16 v3, v109, v7, v3
	v_pk_fma_f16 v4, v110, v8, v4
	v_pk_fma_f16 v5, v111, v9, v5
	v_cndmask_b32_e64 v28, v28, v20, s[66:67]
.Lc1_next0:
	v_pk_fma_f16 v6, v2, v120, v121 op_sel:[0,1,1] op_sel_hi:[1,1,1] neg_lo:[1,0,0] neg_hi:[1,0,0]
	v_pk_fma_f16 v7, v3, v120, v121 op_sel:[0,1,1] op_sel_hi:[1,1,1] neg_lo:[1,0,0] neg_hi:[1,0,0]
	v_pk_fma_f16 v8, v4, v120, v121 op_sel:[0,1,1] op_sel_hi:[1,1,1] neg_lo:[1,0,0] neg_hi:[1,0,0]
	v_pk_fma_f16 v9, v5, v120, v121 op_sel:[0,1,1] op_sel_hi:[1,1,1] neg_lo:[1,0,0] neg_hi:[1,0,0]
	v_mfma_f32_16x16x32_f16 v[18:21], v[14:17], v[2:5], 0
	ds_read2_b64 v[76:79], v32 offset0:23 offset1:225
	ds_read_b128 v[132:135], v33 offset:176
	ds_read_b32 v37, v36 offset:8
	ds_read_b32 v38, v36 offset:72
	v_pk_fma_f16 v2, v48, v6, v2
	v_pk_fma_f16 v3, v49, v7, v3
	v_pk_fma_f16 v4, v50, v8, v4
	v_pk_fma_f16 v5, v51, v9, v5
	v_cndmask_b32_e64 v29, v29, v25, s[66:67]
	v_cvt_pk_f16_f32 v30, v26, v27
	v_cvt_pk_f16_f32 v31, v28, v29
	ds_write_b16 v39, v30 offset:2048
	ds_write_b16_d16_hi v39, v30 offset:2112
	ds_write_b16 v39, v31 offset:2176
	ds_write_b16_d16_hi v39, v31 offset:2240
	s_mov_b64 exec, 1
	ds_add_u32 v36, v44 offset:128
	s_mov_b64 exec, -1
	v_pk_fma_f16 v6, v2, v122, v123 op_sel:[0,1,1] op_sel_hi:[1,1,1] neg_lo:[1,0,0] neg_hi:[1,0,0]
	v_pk_fma_f16 v7, v3, v122, v123 op_sel:[0,1,1] op_sel_hi:[1,1,1] neg_lo:[1,0,0] neg_hi:[1,0,0]
	v_pk_fma_f16 v8, v4, v122, v123 op_sel:[0,1,1] op_sel_hi:[1,1,1] neg_lo:[1,0,0] neg_hi:[1,0,0]
	v_pk_fma_f16 v9, v5, v122, v123 op_sel:[0,1,1] op_sel_hi:[1,1,1] neg_lo:[1,0,0] neg_hi:[1,0,0]
	v_mfma_f32_16x16x32_f16 v[22:25], v[14:17], v[2:5], 0
	ds_read2_b64 v[80:83], v32 offset0:24 offset1:226
	v_pk_fma_f16 v2, v52, v6, v2
	v_pk_fma_f16 v3, v53, v7, v3
	v_pk_fma_f16 v4, v54, v8, v4
	v_pk_fma_f16 v5, v55, v9, v5
	v_cndmask_b32_e64 v26, v26, v18, s[60:61]
	v_pk_fma_f16 v6, v2, v124, v125 op_sel:[0,1,1] op_sel_hi:[1,1,1] neg_lo:[1,0,0] neg_hi:[1,0,0]
	v_pk_fma_f16 v7, v3, v124, v125 op_sel:[0,1,1] op_sel_hi:[1,1,1] neg_lo:[1,0,0] neg_hi:[1,0,0]
	v_pk_fma_f16 v8, v4, v124, v125 op_sel:[0,1,1] op_sel_hi:[1,1,1] neg_lo:[1,0,0] neg_hi:[1,0,0]
	v_pk_fma_f16 v9, v5, v124, v125 op_sel:[0,1,1] op_sel_hi:[1,1,1] neg_lo:[1,0,0] neg_hi:[1,0,0]
	v_mfma_f32_16x16x32_f16 v[18:21], v[14:17], v[2:5], 0
	ds_read2_b64 v[84:87], v32 offset0:25 offset1:227
	ds_read_b128 v[136:139], v33 offset:192
	v_pk_fma_f16 v2, v56, v6, v2
	v_pk_fma_f16 v3, v57, v7, v3
	v_pk_fma_f16 v4, v58, v8, v4
	v_pk_fma_f16 v5, v59, v9, v5
	v_cndmask_b32_e64 v27, v27, v23, s[60:61]
	v_pk_fma_f16 v6, v2, v126, v127 op_sel:[0,1,1] op_sel_hi:[1,1,1] neg_lo:[1,0,0] neg_hi:[1,0,0]
	v_pk_fma_f16 v7, v3, v126, v127 op_sel:[0,1,1] op_sel_hi:[1,1,1] neg_lo:[1,0,0] neg_hi:[1,0,0]
	v_pk_fma_f16 v8, v4, v126, v127 op_sel:[0,1,1] op_sel_hi:[1,1,1] neg_lo:[1,0,0] neg_hi:[1,0,0]
	v_pk_fma_f16 v9, v5, v126, v127 op_sel:[0,1,1] op_sel_hi:[1,1,1] neg_lo:[1,0,0] neg_hi:[1,0,0]
	v_mfma_f32_16x16x32_f16 v[22:25], v[14:17], v[2:5], 0
	ds_read2_b64 v[88:91], v32 offset0:26 offset1:228
	s_waitcnt lgkmcnt(11)
	v_pk_fma_f16 v2, v60, v6, v2
	v_pk_fma_f16 v3, v61, v7, v3
	v_pk_fma_f16 v4, v62, v8, v4
	v_pk_fma_f16 v5, v63, v9, v5
	v_cndmask_b32_e64 v28, v28, v20, s[60:61]
	v_pk_fma_f16 v6, v2, v128, v129 op_sel:[0,1,1] op_sel_hi:[1,1,1] neg_lo:[1,0,0] neg_hi:[1,0,0]
	v_pk_fma_f16 v7, v3, v128, v129 op_sel:[0,1,1] op_sel_hi:[1,1,1] neg_lo:[1,0,0] neg_hi:[1,0,0]
	v_pk_fma_f16 v8, v4, v128, v129 op_sel:[0,1,1] op_sel_hi:[1,1,1] neg_lo:[1,0,0] neg_hi:[1,0,0]
	v_pk_fma_f16 v9, v5, v128, v129 op_sel:[0,1,1] op_sel_hi:[1,1,1] neg_lo:[1,0,0] neg_hi:[1,0,0]
	v_mfma_f32_16x16x32_f16 v[18:21], v[14:17], v[2:5], 0
	ds_read2_b64 v[92:95], v32 offset0:27 offset1:229
	ds_read_b128 v[140:143], v33 offset:208
	v_pk_fma_f16 v2, v64, v6, v2
	v_pk_fma_f16 v3, v65, v7, v3
	v_pk_fma_f16 v4, v66, v8, v4
	v_pk_fma_f16 v5, v67, v9, v5
	v_cndmask_b32_e64 v29, v29, v25, s[60:61]
	v_pk_fma_f16 v6, v2, v130, v131 op_sel:[0,1,1] op_sel_hi:[1,1,1] neg_lo:[1,0,0] neg_hi:[1,0,0]
	v_pk_fma_f16 v7, v3, v130, v131 op_sel:[0,1,1] op_sel_hi:[1,1,1] neg_lo:[1,0,0] neg_hi:[1,0,0]
	v_pk_fma_f16 v8, v4, v130, v131 op_sel:[0,1,1] op_sel_hi:[1,1,1] neg_lo:[1,0,0] neg_hi:[1,0,0]
	v_pk_fma_f16 v9, v5, v130, v131 op_sel:[0,1,1] op_sel_hi:[1,1,1] neg_lo:[1,0,0] neg_hi:[1,0,0]
	v_mfma_f32_16x16x32_f16 v[22:25], v[14:17], v[2:5], 0
	ds_read2_b64 v[96:99], v32 offset0:28 offset1:230
	v_pk_fma_f16 v2, v68, v6, v2
	v_pk_fma_f16 v3, v69, v7, v3
	v_pk_fma_f16 v4, v70, v8, v4
	v_pk_fma_f16 v5, v71, v9, v5
	v_cndmask_b32_e64 v26, v26, v18, s[62:63]
	v_pk_fma_f16 v6, v2, v132, v133 op_sel:[0,1,1] op_sel_hi:[1,1,1] neg_lo:[1,0,0] neg_hi:[1,0,0]
	v_pk_fma_f16 v7, v3, v132, v133 op_sel:[0,1,1] op_sel_hi:[1,1,1] neg_lo:[1,0,0] neg_hi:[1,0,0]
	v_pk_fma_f16 v8, v4, v132, v133 op_sel:[0,1,1] op_sel_hi:[1,1,1] neg_lo:[1,0,0] neg_hi:[1,0,0]
	v_pk_fma_f16 v9, v5, v132, v133 op_sel:[0,1,1] op_sel_hi:[1,1,1] neg_lo:[1,0,0] neg_hi:[1,0,0]
	v_mfma_f32_16x16x32_f16 v[18:21], v[14:17], v[2:5], 0
	ds_read2_b64 v[100:103], v32 offset0:29 offset1:231
	ds_read_b128 v[144:147], v33 offset:224
	v_pk_fma_f16 v2, v72, v6, v2
	v_pk_fma_f16 v3, v73, v7, v3
	v_pk_fma_f16 v4, v74, v8, v4
	v_pk_fma_f16 v5, v75, v9, v5
	v_cndmask_b32_e64 v27, v27, v23, s[62:63]
	v_pk_fma_f16 v6, v2, v134, v135 op_sel:[0,1,1] op_sel_hi:[1,1,1] neg_lo:[1,0,0] neg_hi:[1,0,0]
	v_pk_fma_f16 v7, v3, v134, v135 op_sel:[0,1,1] op_sel_hi:[1,1,1] neg_lo:[1,0,0] neg_hi:[1,0,0]
	v_pk_fma_f16 v8, v4, v134, v135 op_sel:[0,1,1] op_sel_hi:[1,1,1] neg_lo:[1,0,0] neg_hi:[1,0,0]
	v_pk_fma_f16 v9, v5, v134, v135 op_sel:[0,1,1] op_sel_hi:[1,1,1] neg_lo:[1,0,0] neg_hi:[1,0,0]
	v_mfma_f32_16x16x32_f16 v[22:25], v[14:17], v[2:5], 0
	ds_read2_b64 v[104:107], v32 offset0:30 offset1:232
	s_waitcnt lgkmcnt(4)
	v_pk_fma_f16 v2, v76, v6, v2
	v_pk_fma_f16 v3, v77, v7, v3
	v_pk_fma_f16 v4, v78, v8, v4
	v_pk_fma_f16 v5, v79, v9, v5
	v_cndmask_b32_e64 v28, v28, v20, s[62:63]
	v_pk_fma_f16 v6, v2, v136, v137 op_sel:[0,1,1] op_sel_hi:[1,1,1] neg_lo:[1,0,0] neg_hi:[1,0,0]
	v_pk_fma_f16 v7, v3, v136, v137 op_sel:[0,1,1] op_sel_hi:[1,1,1] neg_lo:[1,0,0] neg_hi:[1,0,0]
	v_pk_fma_f16 v8, v4, v136, v137 op_sel:[0,1,1] op_sel_hi:[1,1,1] neg_lo:[1,0,0] neg_hi:[1,0,0]
	v_pk_fma_f16 v9, v5, v136, v137 op_sel:[0,1,1] op_sel_hi:[1,1,1] neg_lo:[1,0,0] neg_hi:[1,0,0]
	v_mfma_f32_16x16x32_f16 v[18:21], v[14:17], v[2:5], 0
	ds_read2_b64 v[108:111], v32 offset0:31 offset1:233
	ds_read_b128 v[148:151], v33 offset:240
	v_pk_fma_f16 v2, v80, v6, v2
	v_pk_fma_f16 v3, v81, v7, v3
	v_pk_fma_f16 v4, v82, v8, v4
	v_pk_fma_f16 v5, v83, v9, v5
	v_cndmask_b32_e64 v29, v29, v25, s[62:63]
	v_readfirstlane_b32 s4, v37
	v_readfirstlane_b32 s5, v38
	s_and_b32 s4, s4, s5
	s_cbranch_scc0 .Lc1_slow1

.Lc1_nd1:
	v_pk_fma_f16 v6, v2, v138, v139 op_sel:[0,1,1] op_sel_hi:[1,1,1] neg_lo:[1,0,0] neg_hi:[1,0,0]
	v_pk_fma_f16 v7, v3, v138, v139 op_sel:[0,1,1] op_sel_hi:[1,1,1] neg_lo:[1,0,0] neg_hi:[1,0,0]
	v_pk_fma_f16 v8, v4, v138, v139 op_sel:[0,1,1] op_sel_hi:[1,1,1] neg_lo:[1,0,0] neg_hi:[1,0,0]
	v_pk_fma_f16 v9, v5, v138, v139 op_sel:[0,1,1] op_sel_hi:[1,1,1] neg_lo:[1,0,0] neg_hi:[1,0,0]
	v_mfma_f32_16x16x32_f16 v[22:25], v[14:17], v[2:5], 0
	ds_read2_b64 v[48:51], v32 offset0:32 offset1:234
	v_pk_fma_f16 v2, v84, v6, v2
	v_pk_fma_f16 v3, v85, v7, v3
	v_pk_fma_f16 v4, v86, v8, v4
	v_pk_fma_f16 v5, v87, v9, v5
	v_cndmask_b32_e64 v26, v26, v18, s[64:65]
	v_pk_fma_f16 v6, v2, v140, v141 op_sel:[0,1,1] op_sel_hi:[1,1,1] neg_lo:[1,0,0] neg_hi:[1,0,0]
	v_pk_fma_f16 v7, v3, v140, v141 op_sel:[0,1,1] op_sel_hi:[1,1,1] neg_lo:[1,0,0] neg_hi:[1,0,0]
	v_pk_fma_f16 v8, v4, v140, v141 op_sel:[0,1,1] op_sel_hi:[1,1,1] neg_lo:[1,0,0] neg_hi:[1,0,0]
	v_pk_fma_f16 v9, v5, v140, v141 op_sel:[0,1,1] op_sel_hi:[1,1,1] neg_lo:[1,0,0] neg_hi:[1,0,0]
	v_mfma_f32_16x16x32_f16 v[18:21], v[14:17], v[2:5], 0
	ds_read2_b64 v[52:55], v32 offset0:33 offset1:235
	ds_read_b128 v[120:123], v33 offset:256
	ds_read2_b64 v[10:13], v34 offset0:32 offset1:234
	v_pk_fma_f16 v2, v88, v6, v2
	v_pk_fma_f16 v3, v89, v7, v3
	v_pk_fma_f16 v4, v90, v8, v4
	v_pk_fma_f16 v5, v91, v9, v5
	v_cndmask_b32_e64 v27, v27, v23, s[64:65]
	v_pk_fma_f16 v6, v2, v142, v143 op_sel:[0,1,1] op_sel_hi:[1,1,1] neg_lo:[1,0,0] neg_hi:[1,0,0]
	v_pk_fma_f16 v7, v3, v142, v143 op_sel:[0,1,1] op_sel_hi:[1,1,1] neg_lo:[1,0,0] neg_hi:[1,0,0]
	v_pk_fma_f16 v8, v4, v142, v143 op_sel:[0,1,1] op_sel_hi:[1,1,1] neg_lo:[1,0,0] neg_hi:[1,0,0]
	v_pk_fma_f16 v9, v5, v142, v143 op_sel:[0,1,1] op_sel_hi:[1,1,1] neg_lo:[1,0,0] neg_hi:[1,0,0]
	v_mfma_f32_16x16x32_f16 v[22:25], v[14:17], v[2:5], 0
	ds_read2_b64 v[56:59], v32 offset0:34 offset1:236
	s_waitcnt lgkmcnt(5)
	v_pk_fma_f16 v2, v92, v6, v2
	v_pk_fma_f16 v3, v93, v7, v3
	v_pk_fma_f16 v4, v94, v8, v4
	v_pk_fma_f16 v5, v95, v9, v5
	v_cndmask_b32_e64 v28, v28, v20, s[64:65]
	v_pk_fma_f16 v6, v2, v144, v145 op_sel:[0,1,1] op_sel_hi:[1,1,1] neg_lo:[1,0,0] neg_hi:[1,0,0]
	v_pk_fma_f16 v7, v3, v144, v145 op_sel:[0,1,1] op_sel_hi:[1,1,1] neg_lo:[1,0,0] neg_hi:[1,0,0]
	v_pk_fma_f16 v8, v4, v144, v145 op_sel:[0,1,1] op_sel_hi:[1,1,1] neg_lo:[1,0,0] neg_hi:[1,0,0]
	v_pk_fma_f16 v9, v5, v144, v145 op_sel:[0,1,1] op_sel_hi:[1,1,1] neg_lo:[1,0,0] neg_hi:[1,0,0]
	v_mfma_f32_16x16x32_f16 v[18:21], v[14:17], v[2:5], 0
	ds_read2_b64 v[60:63], v32 offset0:35 offset1:237
	ds_read_b128 v[124:127], v33 offset:272
	v_pk_fma_f16 v2, v96, v6, v2
	v_pk_fma_f16 v3, v97, v7, v3
	v_pk_fma_f16 v4, v98, v8, v4
	v_pk_fma_f16 v5, v99, v9, v5
	v_cndmask_b32_e64 v29, v29, v25, s[64:65]
	s_cmp_eq_u32 s72, 1
	s_cbranch_scc0 .Lc1_ns1
	s_waitcnt lgkmcnt(7)
	v_readfirstlane_b32 s4, v45
	s_cmp_eq_u32 s4, 4
	s_cbranch_scc0 .Lc1_dslow1

.Lc1_ns1:
	v_pk_fma_f16 v6, v2, v146, v147 op_sel:[0,1,1] op_sel_hi:[1,1,1] neg_lo:[1,0,0] neg_hi:[1,0,0]
	v_pk_fma_f16 v7, v3, v146, v147 op_sel:[0,1,1] op_sel_hi:[1,1,1] neg_lo:[1,0,0] neg_hi:[1,0,0]
	v_pk_fma_f16 v8, v4, v146, v147 op_sel:[0,1,1] op_sel_hi:[1,1,1] neg_lo:[1,0,0] neg_hi:[1,0,0]
	v_pk_fma_f16 v9, v5, v146, v147 op_sel:[0,1,1] op_sel_hi:[1,1,1] neg_lo:[1,0,0] neg_hi:[1,0,0]
	v_mfma_f32_16x16x32_f16 v[22:25], v[14:17], v[2:5], 0
	ds_read2_b64 v[64:67], v32 offset0:36 offset1:238
	v_pk_fma_f16 v2, v100, v6, v2
	v_pk_fma_f16 v3, v101, v7, v3
	v_pk_fma_f16 v4, v102, v8, v4
	v_pk_fma_f16 v5, v103, v9, v5
	v_cndmask_b32_e64 v26, v26, v18, s[66:67]
	v_pk_fma_f16 v6, v2, v148, v149 op_sel:[0,1,1] op_sel_hi:[1,1,1] neg_lo:[1,0,0] neg_hi:[1,0,0]
	v_pk_fma_f16 v7, v3, v148, v149 op_sel:[0,1,1] op_sel_hi:[1,1,1] neg_lo:[1,0,0] neg_hi:[1,0,0]
	v_pk_fma_f16 v8, v4, v148, v149 op_sel:[0,1,1] op_sel_hi:[1,1,1] neg_lo:[1,0,0] neg_hi:[1,0,0]
	v_pk_fma_f16 v9, v5, v148, v149 op_sel:[0,1,1] op_sel_hi:[1,1,1] neg_lo:[1,0,0] neg_hi:[1,0,0]
	v_mfma_f32_16x16x32_f16 v[18:21], v[14:17], v[2:5], 0
	ds_read2_b64 v[68:71], v32 offset0:37 offset1:239
	ds_read_b128 v[128:131], v33 offset:288
	v_pk_fma_f16 v2, v104, v6, v2
	v_pk_fma_f16 v3, v105, v7, v3
	v_pk_fma_f16 v4, v106, v8, v4
	v_pk_fma_f16 v5, v107, v9, v5
	v_cndmask_b32_e64 v27, v27, v23, s[66:67]
	v_pk_fma_f16 v6, v2, v150, v151 op_sel:[0,1,1] op_sel_hi:[1,1,1] neg_lo:[1,0,0] neg_hi:[1,0,0]
	v_pk_fma_f16 v7, v3, v150, v151 op_sel:[0,1,1] op_sel_hi:[1,1,1] neg_lo:[1,0,0] neg_hi:[1,0,0]
	v_pk_fma_f16 v8, v4, v150, v151 op_sel:[0,1,1] op_sel_hi:[1,1,1] neg_lo:[1,0,0] neg_hi:[1,0,0]
	v_pk_fma_f16 v9, v5, v150, v151 op_sel:[0,1,1] op_sel_hi:[1,1,1] neg_lo:[1,0,0] neg_hi:[1,0,0]
	v_mfma_f32_16x16x32_f16 v[22:25], v[14:17], v[2:5], 0
	ds_read2_b64 v[72:75], v32 offset0:38 offset1:240
	s_waitcnt lgkmcnt(4)
	v_pk_fma_f16 v2, v108, v6, v2
	v_pk_fma_f16 v3, v109, v7, v3
	v_pk_fma_f16 v4, v110, v8, v4
	v_pk_fma_f16 v5, v111, v9, v5
	v_cndmask_b32_e64 v28, v28, v20, s[66:67]
.Lc1_next1:
	v_add_u32_e32 v32, 0x100, v32
	v_add_u32_e32 v33, 0x100, v33
	v_add_u32_e32 v34, 0x100, v34
	v_add_u32_e32 v36, 8, v36
	v_add_u32_e32 v39, 0x1000, v39
	v_add_u32_e32 v43, 0x1000, v43
	v_add_u32_e32 v35, 0x800, v35
	s_xor_b32 s71, s71, 2
	s_add_i32 s70, s70, 1
	s_cmp_lt_u32 s70, 6
	s_cbranch_scc1 .Lc1_loop
	v_pk_fma_f16 v6, v2, v120, v121 op_sel:[0,1,1] op_sel_hi:[1,1,1] neg_lo:[1,0,0] neg_hi:[1,0,0]
	v_pk_fma_f16 v7, v3, v120, v121 op_sel:[0,1,1] op_sel_hi:[1,1,1] neg_lo:[1,0,0] neg_hi:[1,0,0]
	v_pk_fma_f16 v8, v4, v120, v121 op_sel:[0,1,1] op_sel_hi:[1,1,1] neg_lo:[1,0,0] neg_hi:[1,0,0]
	v_pk_fma_f16 v9, v5, v120, v121 op_sel:[0,1,1] op_sel_hi:[1,1,1] neg_lo:[1,0,0] neg_hi:[1,0,0]
	v_mfma_f32_16x16x32_f16 v[18:21], v[10:13], v[2:5], 0
	ds_read2_b64 v[76:79], v32 offset0:7 offset1:209
	ds_read_b128 v[132:135], v33 offset:48
	v_pk_fma_f16 v2, v48, v6, v2
	v_pk_fma_f16 v3, v49, v7, v3
	v_pk_fma_f16 v4, v50, v8, v4
	v_pk_fma_f16 v5, v51, v9, v5
	v_cndmask_b32_e64 v29, v29, v25, s[66:67]
	v_cvt_pk_f16_f32 v30, v26, v27
	v_cvt_pk_f16_f32 v31, v28, v29
	ds_write_b16 v39, v30 offset:0
	ds_write_b16_d16_hi v39, v30 offset:64
	ds_write_b16 v39, v31 offset:128
	ds_write_b16_d16_hi v39, v31 offset:192
	s_mov_b64 exec, 1
	ds_add_u32 v36, v44 offset:124
	s_mov_b64 exec, -1
	v_pk_fma_f16 v6, v2, v122, v123 op_sel:[0,1,1] op_sel_hi:[1,1,1] neg_lo:[1,0,0] neg_hi:[1,0,0]
	v_pk_fma_f16 v7, v3, v122, v123 op_sel:[0,1,1] op_sel_hi:[1,1,1] neg_lo:[1,0,0] neg_hi:[1,0,0]
	v_pk_fma_f16 v8, v4, v122, v123 op_sel:[0,1,1] op_sel_hi:[1,1,1] neg_lo:[1,0,0] neg_hi:[1,0,0]
	v_pk_fma_f16 v9, v5, v122, v123 op_sel:[0,1,1] op_sel_hi:[1,1,1] neg_lo:[1,0,0] neg_hi:[1,0,0]
	v_mfma_f32_16x16x32_f16 v[22:25], v[10:13], v[2:5], 0
	v_pk_fma_f16 v2, v52, v6, v2
	v_pk_fma_f16 v3, v53, v7, v3
	v_pk_fma_f16 v4, v54, v8, v4
	v_pk_fma_f16 v5, v55, v9, v5
	v_cndmask_b32_e64 v26, v26, v18, s[60:61]
	v_pk_fma_f16 v6, v2, v124, v125 op_sel:[0,1,1] op_sel_hi:[1,1,1] neg_lo:[1,0,0] neg_hi:[1,0,0]
	v_pk_fma_f16 v7, v3, v124, v125 op_sel:[0,1,1] op_sel_hi:[1,1,1] neg_lo:[1,0,0] neg_hi:[1,0,0]
	v_pk_fma_f16 v8, v4, v124, v125 op_sel:[0,1,1] op_sel_hi:[1,1,1] neg_lo:[1,0,0] neg_hi:[1,0,0]
	v_pk_fma_f16 v9, v5, v124, v125 op_sel:[0,1,1] op_sel_hi:[1,1,1] neg_lo:[1,0,0] neg_hi:[1,0,0]
	v_mfma_f32_16x16x32_f16 v[18:21], v[10:13], v[2:5], 0
	v_pk_fma_f16 v2, v56, v6, v2
	v_pk_fma_f16 v3, v57, v7, v3
	v_pk_fma_f16 v4, v58, v8, v4
	v_pk_fma_f16 v5, v59, v9, v5
	v_cndmask_b32_e64 v27, v27, v23, s[60:61]
	v_pk_fma_f16 v6, v2, v126, v127 op_sel:[0,1,1] op_sel_hi:[1,1,1] neg_lo:[1,0,0] neg_hi:[1,0,0]
	v_pk_fma_f16 v7, v3, v126, v127 op_sel:[0,1,1] op_sel_hi:[1,1,1] neg_lo:[1,0,0] neg_hi:[1,0,0]
	v_pk_fma_f16 v8, v4, v126, v127 op_sel:[0,1,1] op_sel_hi:[1,1,1] neg_lo:[1,0,0] neg_hi:[1,0,0]
	v_pk_fma_f16 v9, v5, v126, v127 op_sel:[0,1,1] op_sel_hi:[1,1,1] neg_lo:[1,0,0] neg_hi:[1,0,0]
	v_mfma_f32_16x16x32_f16 v[22:25], v[10:13], v[2:5], 0
	s_waitcnt lgkmcnt(5)
	v_pk_fma_f16 v2, v60, v6, v2
	v_pk_fma_f16 v3, v61, v7, v3
	v_pk_fma_f16 v4, v62, v8, v4
	v_pk_fma_f16 v5, v63, v9, v5
	v_cndmask_b32_e64 v28, v28, v20, s[60:61]
	s_mov_b32 s72, 0
	s_cmp_eq_u32 s70, 0
	s_cbranch_scc1 .Lc1_ndt
	s_cmp_eq_u32 s36, 3
	s_cbranch_scc0 .Lc1_ndt
	s_mov_b32 s72, 1
	ds_read_b32 v45, v36 offset:124
	ds_read_b128 v[112:115], v43 offset:0
	ds_read_b128 v[116:119], v43 offset:1024
